# cache policy: non-temporal (nt) hint on the once-read f32 weight loads of the conversion units so the stream stops evicting reused tiles from L2
# speedup vs baseline: 1.0048x; 1.0048x over previous
; #define LAS __attribute__((address_space(3)))
; #define LDS_WAIT() asm volatile("s_waitcnt lgkmcnt(0)" ::: "memory")
; __device__ __forceinline__ void p0_transpose_item8(const float* W, int ldw, int srccol0, int k0, unsigned char* dst, int K, LAS float* scr, int lane) {
;     { f32x4 v[8];
; #pragma unroll
;       for (int i = 0; i < 8; ++i) v[i] = *(const f32x4*)(W + (size_t)(k0 + 8 * i + (lane >> 3)) * ldw + srccol0 + 4 * (lane & 7));
; #pragma unroll
;       for (int i = 0; i < 8; ++i) { LAS float* p = scr + (8 * i + (lane >> 3)) * 33 + 4 * (lane & 7); p[0] = v[i][0]; p[1] = v[i][1]; p[2] = v[i][2]; p[3] = v[i][3]; } }
;     LDS_WAIT(); asm volatile("" ::: "memory");
; __device__ __forceinline__ void p0_item(KP Pk, Frame& F, int it, LAS float* scr) {
;     ...
;     { const int le = it / TI_DN, r = it % TI_DN, kb = r / 64, nb = r % 64;
;         p0_transpose_item8(Pk->in[I_ED] + (size_t)le * DE * D, D, 32 * nb, 64 * kb, ws + WS_WD + ((size_t)le * D + 32 * nb) * DE, DE, scr, F.lane); }
.Lcv_dn:
	s_load_dwordx2 s[8:9], s[48:49], 0x108
	s_add_i32 s5, s4, 0xfffec5c0
	s_lshr_b32 s60, s5, 10
	s_and_b32 s5, s5, 0x3c0
	s_lshl_b64 s[18:19], s[60:61], 23
	s_waitcnt lgkmcnt(0)
	s_add_u32 s18, s8, s18
	s_addc_u32 s19, s9, s19
	s_lshl_b32 s8, s4, 5
	s_and_b32 s26, s8, 0x7e0
	s_lshl_b64 s[8:9], s[60:61], 21
	s_lshl_b32 s27, s26, 10
	v_readlane_b32 s34, v255, 7
	s_add_u32 s8, s34, s8
	v_readlane_b32 s34, v255, 8
	s_addc_u32 s9, s34, s9
	s_add_u32 s8, s8, s27
	s_addc_u32 s9, s9, 0
	s_add_u32 s8, s8, s5
	s_addc_u32 s9, s9, 0
	s_lshl_b32 s26, s26, 2
	s_add_u32 s18, s18, s26
	s_addc_u32 s19, s19, 0
	v_add_u32_e32 v32, s5, v2
	v_lshlrev_b32_e32 v32, 13, v32
	v_lshl_add_u32 v68, v4, 2, v32
	v_add_u32_e32 v69, 0x10000, v68
	v_add_u32_e32 v70, 0x20000, v68
	v_add_u32_e32 v71, 0x30000, v68
	v_add_u32_e32 v72, 0x40000, v68
	v_add_u32_e32 v73, 0x50000, v68
	v_add_u32_e32 v74, 0x60000, v68
	v_add_u32_e32 v75, 0x70000, v68
	global_load_dwordx4 v[84:87], v68, s[18:19] nt
	global_load_dwordx4 v[88:91], v69, s[18:19] nt
	global_load_dwordx4 v[92:95], v70, s[18:19] nt
	global_load_dwordx4 v[96:99], v71, s[18:19] nt
	global_load_dwordx4 v[100:103], v72, s[18:19] nt
	global_load_dwordx4 v[104:107], v73, s[18:19] nt
	global_load_dwordx4 v[108:111], v74, s[18:19] nt
	global_load_dwordx4 v[112:115], v75, s[18:19] nt
	global_load_dwordx4 v[116:119], v68, s[18:19] offset:128 nt
	global_load_dwordx4 v[120:123], v69, s[18:19] offset:128 nt
	global_load_dwordx4 v[124:127], v70, s[18:19] offset:128 nt
	global_load_dwordx4 v[128:131], v71, s[18:19] offset:128 nt
	global_load_dwordx4 v[132:135], v72, s[18:19] offset:128 nt
	global_load_dwordx4 v[136:139], v73, s[18:19] offset:128 nt
	global_load_dwordx4 v[140:143], v74, s[18:19] offset:128 nt
	global_load_dwordx4 v[144:147], v75, s[18:19] offset:128 nt
	global_load_dwordx4 v[148:151], v68, s[18:19] offset:256 nt
	global_load_dwordx4 v[152:155], v69, s[18:19] offset:256 nt
	global_load_dwordx4 v[156:159], v70, s[18:19] offset:256 nt
	global_load_dwordx4 v[160:163], v71, s[18:19] offset:256 nt
	global_load_dwordx4 v[164:167], v72, s[18:19] offset:256 nt
	global_load_dwordx4 v[168:171], v73, s[18:19] offset:256 nt
	global_load_dwordx4 v[178:181], v74, s[18:19] offset:256 nt
	global_load_dwordx4 v[182:185], v75, s[18:19] offset:256 nt
	global_load_dwordx4 v[196:199], v68, s[18:19] offset:384 nt
	global_load_dwordx4 v[200:203], v69, s[18:19] offset:384 nt
	global_load_dwordx4 v[204:207], v70, s[18:19] offset:384 nt
	global_load_dwordx4 v[208:211], v71, s[18:19] offset:384 nt
	global_load_dwordx4 v[212:215], v72, s[18:19] offset:384 nt
	global_load_dwordx4 v[216:219], v73, s[18:19] offset:384 nt
	global_load_dwordx4 v[220:223], v74, s[18:19] offset:384 nt
	global_load_dwordx4 v[186:189], v75, s[18:19] offset:384 nt
	s_add_u32 s18, s18, 0x200
	s_addc_u32 s19, s19, 0
	s_mov_b32 s43, 0

; #define LAS __attribute__((address_space(3)))
; #define LDS_WAIT() asm volatile("s_waitcnt lgkmcnt(0)" ::: "memory")
; __device__ __forceinline__ void p0_transpose_item8(const float* W, int ldw, int srccol0, int k0, unsigned char* dst, int K, LAS float* scr, int lane) {
;     { f32x4 v[8];
; #pragma unroll
;       for (int i = 0; i < 8; ++i) v[i] = *(const f32x4*)(W + (size_t)(k0 + 8 * i + (lane >> 3)) * ldw + srccol0 + 4 * (lane & 7));
; #pragma unroll
;       for (int i = 0; i < 8; ++i) { LAS float* p = scr + (8 * i + (lane >> 3)) * 33 + 4 * (lane & 7); p[0] = v[i][0]; p[1] = v[i][1]; p[2] = v[i][2]; p[3] = v[i][3]; } }
;     LDS_WAIT(); asm volatile("" ::: "memory");
.Lcv_dn_0_d:
	v_add_u32_e32 v3, v1, v5
	ds_write2_b32 v3, v84, v85 offset1:1
	ds_write2_b32 v3, v86, v87 offset0:2 offset1:3
	v_add_u32_e32 v32, 0x420, v3
	ds_write2_b32 v32, v88, v89 offset1:1
	v_add_u32_e32 v33, 0x428, v3
	ds_write2_b32 v33, v90, v91 offset1:1
	v_add_u32_e32 v32, 0x840, v3
	ds_write2_b32 v32, v92, v93 offset1:1
	v_add_u32_e32 v33, 0x848, v3
	ds_write2_b32 v33, v94, v95 offset1:1
	v_add_u32_e32 v32, 0xc60, v3
	ds_write2_b32 v32, v96, v97 offset1:1
	v_add_u32_e32 v33, 0xc68, v3
	ds_write2_b32 v33, v98, v99 offset1:1
	v_add_u32_e32 v32, 0x1080, v3
	ds_write2_b32 v32, v100, v101 offset1:1
	v_add_u32_e32 v33, 0x1088, v3
	ds_write2_b32 v33, v102, v103 offset1:1
	v_add_u32_e32 v32, 0x14a0, v3
	ds_write2_b32 v32, v104, v105 offset1:1
	v_add_u32_e32 v33, 0x14a8, v3
	ds_write2_b32 v33, v106, v107 offset1:1
	v_add_u32_e32 v32, 0x18c0, v3
	ds_write2_b32 v32, v108, v109 offset1:1
	v_add_u32_e32 v33, 0x18c8, v3
	ds_write2_b32 v33, v110, v111 offset1:1
	v_add_u32_e32 v32, 0x1ce0, v3
	ds_write2_b32 v32, v112, v113 offset1:1
	v_add_u32_e32 v33, 0x1ce8, v3
	ds_write2_b32 v33, v114, v115 offset1:1
	v_mov_b32_e32 v42, v0
	v_mov_b32_e32 v43, v0
	s_waitcnt lgkmcnt(0)
	s_cmp_lt_u32 s43, 12
	s_cbranch_scc0 .Lcv_dn_0_n
	global_load_dwordx4 v[84:87], v68, s[18:19] nt
	global_load_dwordx4 v[88:91], v69, s[18:19] nt
	global_load_dwordx4 v[92:95], v70, s[18:19] nt
	global_load_dwordx4 v[96:99], v71, s[18:19] nt
	global_load_dwordx4 v[100:103], v72, s[18:19] nt
	global_load_dwordx4 v[104:107], v73, s[18:19] nt
	global_load_dwordx4 v[108:111], v74, s[18:19] nt
	global_load_dwordx4 v[112:115], v75, s[18:19] nt

; #define LAS __attribute__((address_space(3)))
; #define LDS_WAIT() asm volatile("s_waitcnt lgkmcnt(0)" ::: "memory")
; __device__ __forceinline__ void p0_transpose_item8(const float* W, int ldw, int srccol0, int k0, unsigned char* dst, int K, LAS float* scr, int lane) {
;     { f32x4 v[8];
; #pragma unroll
;       for (int i = 0; i < 8; ++i) v[i] = *(const f32x4*)(W + (size_t)(k0 + 8 * i + (lane >> 3)) * ldw + srccol0 + 4 * (lane & 7));
; #pragma unroll
;       for (int i = 0; i < 8; ++i) { LAS float* p = scr + (8 * i + (lane >> 3)) * 33 + 4 * (lane & 7); p[0] = v[i][0]; p[1] = v[i][1]; p[2] = v[i][2]; p[3] = v[i][3]; } }
;     LDS_WAIT(); asm volatile("" ::: "memory");
.Lcv_dn_1_d:
	v_add_u32_e32 v3, v1, v5
	ds_write2_b32 v3, v116, v117 offset1:1
	ds_write2_b32 v3, v118, v119 offset0:2 offset1:3
	v_add_u32_e32 v32, 0x420, v3
	ds_write2_b32 v32, v120, v121 offset1:1
	v_add_u32_e32 v33, 0x428, v3
	ds_write2_b32 v33, v122, v123 offset1:1
	v_add_u32_e32 v32, 0x840, v3
	ds_write2_b32 v32, v124, v125 offset1:1
	v_add_u32_e32 v33, 0x848, v3
	ds_write2_b32 v33, v126, v127 offset1:1
	v_add_u32_e32 v32, 0xc60, v3
	ds_write2_b32 v32, v128, v129 offset1:1
	v_add_u32_e32 v33, 0xc68, v3
	ds_write2_b32 v33, v130, v131 offset1:1
	v_add_u32_e32 v32, 0x1080, v3
	ds_write2_b32 v32, v132, v133 offset1:1
	v_add_u32_e32 v33, 0x1088, v3
	ds_write2_b32 v33, v134, v135 offset1:1
	v_add_u32_e32 v32, 0x14a0, v3
	ds_write2_b32 v32, v136, v137 offset1:1
	v_add_u32_e32 v33, 0x14a8, v3
	ds_write2_b32 v33, v138, v139 offset1:1
	v_add_u32_e32 v32, 0x18c0, v3
	ds_write2_b32 v32, v140, v141 offset1:1
	v_add_u32_e32 v33, 0x18c8, v3
	ds_write2_b32 v33, v142, v143 offset1:1
	v_add_u32_e32 v32, 0x1ce0, v3
	ds_write2_b32 v32, v144, v145 offset1:1
	v_add_u32_e32 v33, 0x1ce8, v3
	ds_write2_b32 v33, v146, v147 offset1:1
	v_mov_b32_e32 v42, v0
	v_mov_b32_e32 v43, v0
	s_waitcnt lgkmcnt(0)
	s_cmp_lt_u32 s43, 12
	s_cbranch_scc0 .Lcv_dn_1_n
	global_load_dwordx4 v[116:119], v68, s[18:19] offset:128 nt
	global_load_dwordx4 v[120:123], v69, s[18:19] offset:128 nt
	global_load_dwordx4 v[124:127], v70, s[18:19] offset:128 nt
	global_load_dwordx4 v[128:131], v71, s[18:19] offset:128 nt
	global_load_dwordx4 v[132:135], v72, s[18:19] offset:128 nt
	global_load_dwordx4 v[136:139], v73, s[18:19] offset:128 nt
	global_load_dwordx4 v[140:143], v74, s[18:19] offset:128 nt
	global_load_dwordx4 v[144:147], v75, s[18:19] offset:128 nt

; #define LAS __attribute__((address_space(3)))
; #define LDS_WAIT() asm volatile("s_waitcnt lgkmcnt(0)" ::: "memory")
; __device__ __forceinline__ void p0_transpose_item8(const float* W, int ldw, int srccol0, int k0, unsigned char* dst, int K, LAS float* scr, int lane) {
;     { f32x4 v[8];
; #pragma unroll
;       for (int i = 0; i < 8; ++i) v[i] = *(const f32x4*)(W + (size_t)(k0 + 8 * i + (lane >> 3)) * ldw + srccol0 + 4 * (lane & 7));
; #pragma unroll
;       for (int i = 0; i < 8; ++i) { LAS float* p = scr + (8 * i + (lane >> 3)) * 33 + 4 * (lane & 7); p[0] = v[i][0]; p[1] = v[i][1]; p[2] = v[i][2]; p[3] = v[i][3]; } }
;     LDS_WAIT(); asm volatile("" ::: "memory");
.Lcv_dn_2_d:
	v_add_u32_e32 v3, v1, v5
	ds_write2_b32 v3, v148, v149 offset1:1
	ds_write2_b32 v3, v150, v151 offset0:2 offset1:3
	v_add_u32_e32 v32, 0x420, v3
	ds_write2_b32 v32, v152, v153 offset1:1
	v_add_u32_e32 v33, 0x428, v3
	ds_write2_b32 v33, v154, v155 offset1:1
	v_add_u32_e32 v32, 0x840, v3
	ds_write2_b32 v32, v156, v157 offset1:1
	v_add_u32_e32 v33, 0x848, v3
	ds_write2_b32 v33, v158, v159 offset1:1
	v_add_u32_e32 v32, 0xc60, v3
	ds_write2_b32 v32, v160, v161 offset1:1
	v_add_u32_e32 v33, 0xc68, v3
	ds_write2_b32 v33, v162, v163 offset1:1
	v_add_u32_e32 v32, 0x1080, v3
	ds_write2_b32 v32, v164, v165 offset1:1
	v_add_u32_e32 v33, 0x1088, v3
	ds_write2_b32 v33, v166, v167 offset1:1
	v_add_u32_e32 v32, 0x14a0, v3
	ds_write2_b32 v32, v168, v169 offset1:1
	v_add_u32_e32 v33, 0x14a8, v3
	ds_write2_b32 v33, v170, v171 offset1:1
	v_add_u32_e32 v32, 0x18c0, v3
	ds_write2_b32 v32, v178, v179 offset1:1
	v_add_u32_e32 v33, 0x18c8, v3
	ds_write2_b32 v33, v180, v181 offset1:1
	v_add_u32_e32 v32, 0x1ce0, v3
	ds_write2_b32 v32, v182, v183 offset1:1
	v_add_u32_e32 v33, 0x1ce8, v3
	ds_write2_b32 v33, v184, v185 offset1:1
	v_mov_b32_e32 v42, v0
	v_mov_b32_e32 v43, v0
	s_waitcnt lgkmcnt(0)
	s_cmp_lt_u32 s43, 12
	s_cbranch_scc0 .Lcv_dn_2_n
	global_load_dwordx4 v[148:151], v68, s[18:19] offset:256 nt
	global_load_dwordx4 v[152:155], v69, s[18:19] offset:256 nt
	global_load_dwordx4 v[156:159], v70, s[18:19] offset:256 nt
	global_load_dwordx4 v[160:163], v71, s[18:19] offset:256 nt
	global_load_dwordx4 v[164:167], v72, s[18:19] offset:256 nt
	global_load_dwordx4 v[168:171], v73, s[18:19] offset:256 nt
	global_load_dwordx4 v[178:181], v74, s[18:19] offset:256 nt
	global_load_dwordx4 v[182:185], v75, s[18:19] offset:256 nt

; #define LAS __attribute__((address_space(3)))
; #define LDS_WAIT() asm volatile("s_waitcnt lgkmcnt(0)" ::: "memory")
; __device__ __forceinline__ void p0_transpose_item8(const float* W, int ldw, int srccol0, int k0, unsigned char* dst, int K, LAS float* scr, int lane) {
;     { f32x4 v[8];
; #pragma unroll
;       for (int i = 0; i < 8; ++i) v[i] = *(const f32x4*)(W + (size_t)(k0 + 8 * i + (lane >> 3)) * ldw + srccol0 + 4 * (lane & 7));
; #pragma unroll
;       for (int i = 0; i < 8; ++i) { LAS float* p = scr + (8 * i + (lane >> 3)) * 33 + 4 * (lane & 7); p[0] = v[i][0]; p[1] = v[i][1]; p[2] = v[i][2]; p[3] = v[i][3]; } }
;     LDS_WAIT(); asm volatile("" ::: "memory");
.Lcv_dn_3_d:
	v_add_u32_e32 v3, v1, v5
	ds_write2_b32 v3, v196, v197 offset1:1
	ds_write2_b32 v3, v198, v199 offset0:2 offset1:3
	v_add_u32_e32 v32, 0x420, v3
	ds_write2_b32 v32, v200, v201 offset1:1
	v_add_u32_e32 v33, 0x428, v3
	ds_write2_b32 v33, v202, v203 offset1:1
	v_add_u32_e32 v32, 0x840, v3
	ds_write2_b32 v32, v204, v205 offset1:1
	v_add_u32_e32 v33, 0x848, v3
	ds_write2_b32 v33, v206, v207 offset1:1
	v_add_u32_e32 v32, 0xc60, v3
	ds_write2_b32 v32, v208, v209 offset1:1
	v_add_u32_e32 v33, 0xc68, v3
	ds_write2_b32 v33, v210, v211 offset1:1
	v_add_u32_e32 v32, 0x1080, v3
	ds_write2_b32 v32, v212, v213 offset1:1
	v_add_u32_e32 v33, 0x1088, v3
	ds_write2_b32 v33, v214, v215 offset1:1
	v_add_u32_e32 v32, 0x14a0, v3
	ds_write2_b32 v32, v216, v217 offset1:1
	v_add_u32_e32 v33, 0x14a8, v3
	ds_write2_b32 v33, v218, v219 offset1:1
	v_add_u32_e32 v32, 0x18c0, v3
	ds_write2_b32 v32, v220, v221 offset1:1
	v_add_u32_e32 v33, 0x18c8, v3
	ds_write2_b32 v33, v222, v223 offset1:1
	v_add_u32_e32 v32, 0x1ce0, v3
	ds_write2_b32 v32, v186, v187 offset1:1
	v_add_u32_e32 v33, 0x1ce8, v3
	ds_write2_b32 v33, v188, v189 offset1:1
	v_mov_b32_e32 v42, v0
	v_mov_b32_e32 v43, v0
	s_waitcnt lgkmcnt(0)
	s_cmp_lt_u32 s43, 12
	s_cbranch_scc0 .Lcv_dn_3_n
	global_load_dwordx4 v[196:199], v68, s[18:19] offset:384 nt
	global_load_dwordx4 v[200:203], v69, s[18:19] offset:384 nt
	global_load_dwordx4 v[204:207], v70, s[18:19] offset:384 nt
	global_load_dwordx4 v[208:211], v71, s[18:19] offset:384 nt
	global_load_dwordx4 v[212:215], v72, s[18:19] offset:384 nt
	global_load_dwordx4 v[216:219], v73, s[18:19] offset:384 nt
	global_load_dwordx4 v[220:223], v74, s[18:19] offset:384 nt
	global_load_dwordx4 v[186:189], v75, s[18:19] offset:384 nt

; #define LAS __attribute__((address_space(3)))
; __device__ __forceinline__ void p0_transpose_item8(const float* W, int ldw, int srccol0, int k0, unsigned char* dst, int K, LAS float* scr, int lane) {
;     { f32x4 v[8];
; #pragma unroll
;       for (int i = 0; i < 8; ++i) v[i] = *(const f32x4*)(W + (size_t)(k0 + 8 * i + (lane >> 3)) * ldw + srccol0 + 4 * (lane & 7));
; __device__ __forceinline__ void p0_item(KP Pk, Frame& F, int it, LAS float* scr) {
;     ...
;     if (it < 32 * TI_GU) { const int le = it / TI_GU, r = it % TI_GU, kb = r / 64, nb = r % 64, n0 = 32 * nb, j = n0 >> 8, half = (n0 >> 7) & 1, c0 = 128 * j + (n0 & 127);
;         p0_transpose_item8((half ? Pk->in[I_EU] : Pk->in[I_EG]) + (size_t)le * D * DE, DE, c0, 64 * kb, ws + WS_WGU + ((size_t)le * 2048 + n0) * D, D, scr, F.lane); return; }
.Lcv_gu:
	s_load_dwordx2 s[18:19], s[48:49], 0xf8
	s_load_dwordx2 s[26:27], s[48:49], 0x100
	s_add_i32 s5, s4, 0xffffc5c0
	s_and_b32 s60, s5, 0xfffff800
	s_and_b32 s34, s5, 0x7c0
	s_lshl_b32 s8, s4, 5
	s_and_b32 s8, s8, 0x7e0
	s_lshl_b32 s9, s4, 4
	s_and_b32 s9, s9, 0x380
	s_lshl_b32 s5, s4, 5
	s_and_b32 s5, s5, 0x60
	s_or_b32 s5, s9, s5
	s_lshl_b32 s5, s5, 2
	s_or_b32 s8, s60, s8
	s_mov_b32 s9, 0
	s_lshl_b64 s[8:9], s[8:9], 11
	v_readlane_b32 s4, v255, 9
	s_add_u32 s8, s4, s8
	v_readlane_b32 s4, v255, 10
	s_addc_u32 s9, s4, s9
	s_add_u32 s8, s8, s34
	s_addc_u32 s9, s9, 0
	s_lshl_b32 s60, s60, 12
	s_add_u32 s60, s60, s5
	s_waitcnt lgkmcnt(0)
	s_add_u32 s18, s18, s60
	s_addc_u32 s19, s19, 0
	s_add_u32 s26, s26, s60
	s_addc_u32 s27, s27, 0
	v_add_u32_e32 v32, s34, v2
	v_lshlrev_b32_e32 v32, 12, v32
	v_lshl_add_u32 v68, v4, 2, v32
	v_add_u32_e32 v69, 0x8000, v68
	v_add_u32_e32 v70, 0x10000, v68
	v_add_u32_e32 v71, 0x18000, v68
	v_add_u32_e32 v72, 0x20000, v68
	v_add_u32_e32 v73, 0x28000, v68
	v_add_u32_e32 v74, 0x30000, v68
	v_add_u32_e32 v75, 0x38000, v68
	global_load_dwordx4 v[84:87], v68, s[18:19] nt
	global_load_dwordx4 v[88:91], v69, s[18:19] nt
	global_load_dwordx4 v[92:95], v70, s[18:19] nt
	global_load_dwordx4 v[96:99], v71, s[18:19] nt
	global_load_dwordx4 v[100:103], v72, s[18:19] nt
	global_load_dwordx4 v[104:107], v73, s[18:19] nt
	global_load_dwordx4 v[108:111], v74, s[18:19] nt
	global_load_dwordx4 v[112:115], v75, s[18:19] nt
	global_load_dwordx4 v[116:119], v68, s[18:19] offset:128 nt
	global_load_dwordx4 v[120:123], v69, s[18:19] offset:128 nt
	global_load_dwordx4 v[124:127], v70, s[18:19] offset:128 nt
	global_load_dwordx4 v[128:131], v71, s[18:19] offset:128 nt
	global_load_dwordx4 v[132:135], v72, s[18:19] offset:128 nt
	global_load_dwordx4 v[136:139], v73, s[18:19] offset:128 nt
	global_load_dwordx4 v[140:143], v74, s[18:19] offset:128 nt
	global_load_dwordx4 v[144:147], v75, s[18:19] offset:128 nt
	global_load_dwordx4 v[148:151], v68, s[18:19] offset:256 nt
	global_load_dwordx4 v[152:155], v69, s[18:19] offset:256 nt
	global_load_dwordx4 v[156:159], v70, s[18:19] offset:256 nt
	global_load_dwordx4 v[160:163], v71, s[18:19] offset:256 nt
	global_load_dwordx4 v[164:167], v72, s[18:19] offset:256 nt
	global_load_dwordx4 v[168:171], v73, s[18:19] offset:256 nt
	global_load_dwordx4 v[178:181], v74, s[18:19] offset:256 nt
	global_load_dwordx4 v[182:185], v75, s[18:19] offset:256 nt
	global_load_dwordx4 v[196:199], v68, s[18:19] offset:384 nt
	global_load_dwordx4 v[200:203], v69, s[18:19] offset:384 nt
	global_load_dwordx4 v[204:207], v70, s[18:19] offset:384 nt
	global_load_dwordx4 v[208:211], v71, s[18:19] offset:384 nt
	global_load_dwordx4 v[212:215], v72, s[18:19] offset:384 nt
	global_load_dwordx4 v[216:219], v73, s[18:19] offset:384 nt
	global_load_dwordx4 v[220:223], v74, s[18:19] offset:384 nt
	global_load_dwordx4 v[186:189], v75, s[18:19] offset:384 nt
	s_mov_b32 s4, s18
	s_mov_b32 s5, s19
	s_mov_b32 s18, s26
	s_mov_b32 s19, s27
	s_add_u32 s26, s4, 0x200
	s_addc_u32 s27, s5, 0
	s_mov_b32 s43, 0

; #define LAS __attribute__((address_space(3)))
; #define LDS_WAIT() asm volatile("s_waitcnt lgkmcnt(0)" ::: "memory")
; __device__ __forceinline__ void p0_transpose_item8(const float* W, int ldw, int srccol0, int k0, unsigned char* dst, int K, LAS float* scr, int lane) {
;     { f32x4 v[8];
; #pragma unroll
;       for (int i = 0; i < 8; ++i) v[i] = *(const f32x4*)(W + (size_t)(k0 + 8 * i + (lane >> 3)) * ldw + srccol0 + 4 * (lane & 7));
; #pragma unroll
;       for (int i = 0; i < 8; ++i) { LAS float* p = scr + (8 * i + (lane >> 3)) * 33 + 4 * (lane & 7); p[0] = v[i][0]; p[1] = v[i][1]; p[2] = v[i][2]; p[3] = v[i][3]; } }
;     LDS_WAIT(); asm volatile("" ::: "memory");
;     const int c = lane & 7;
; #pragma unroll
;     for (int j = 0; j < 4; ++j) { const int n = (lane >> 3) + 8 * j; const LAS float* s = scr + (8 * c) * 33 + n;
;         u32x2 o; o.x = pk4_f8(s[0 * 33] * 32.f, s[1 * 33] * 32.f, s[2 * 33] * 32.f, s[3 * 33] * 32.f); o.y = pk4_f8(s[4 * 33] * 32.f, s[5 * 33] * 32.f, s[6 * 33] * 32.f, s[7 * 33] * 32.f);
;         *(u32x2*)(dst + (size_t)n * K + k0 + 8 * c) = o; }
;     LDS_WAIT(); asm volatile("" ::: "memory");
; __device__ __forceinline__ void p0_item(KP Pk, Frame& F, int it, LAS float* scr) {
;     ...
;     { const int le = it / TI_DN, r = it % TI_DN, kb = r / 64, nb = r % 64;
;         p0_transpose_item8(Pk->in[I_ED] + (size_t)le * DE * D, D, 32 * nb, 64 * kb, ws + WS_WD + ((size_t)le * D + 32 * nb) * DE, DE, scr, F.lane); }
.LBB0_836:
	s_cmp_gt_u32 s4, 0x13a3f
	s_cbranch_scc0 .LBB0_838
	s_cmp_eq_u32 s43, 0
	s_cbranch_scc1 .Lcv_dn
	s_load_dwordx2 s[8:9], s[48:49], 0x108
	s_add_i32 s5, s4, 0xfffec5c0
	s_lshr_b32 s60, s5, 10
	s_and_b32 s5, s5, 0x3c0
	s_lshl_b64 s[18:19], s[60:61], 23
	s_waitcnt lgkmcnt(0)
	s_add_u32 s18, s8, s18
	s_addc_u32 s19, s9, s19
	s_lshl_b32 s8, s4, 5
	s_and_b32 s26, s8, 0x7e0
	s_lshl_b64 s[8:9], s[60:61], 21
	s_lshl_b32 s27, s26, 10
	v_readlane_b32 s34, v255, 7
	s_add_u32 s8, s34, s8
	v_readlane_b32 s34, v255, 8
	s_addc_u32 s9, s34, s9
	s_add_u32 s27, s8, s27
	s_addc_u32 s34, s9, 0
	s_lshl_b32 s8, s26, 2
	v_add_u32_e32 v32, s5, v2
	s_add_u32 s8, s18, s8
	s_addc_u32 s9, s19, 0
	v_lshlrev_b32_e32 v34, 2, v4
	v_mov_b32_e32 v35, v0
	v_ashrrev_i32_e32 v33, 31, v32
	v_lshl_add_u64 v[34:35], s[8:9], 0, v[34:35]
	v_lshlrev_b64 v[32:33], 13, v[32:33]
	v_lshl_add_u64 v[48:49], v[34:35], 0, v[32:33]
	s_mov_b32 s8, 0x10000
	v_add_co_u32_e32 v36, vcc, s8, v48
	global_load_dwordx4 v[32:35], v[48:49], off nt
	s_nop 0
	v_addc_co_u32_e32 v37, vcc, 0, v49, vcc
	s_mov_b32 s8, 0x20000
	global_load_dwordx4 v[36:39], v[36:37], off nt
	v_add_co_u32_e32 v40, vcc, s8, v48
	s_mov_b32 s8, 0x30000
	s_nop 0
	v_addc_co_u32_e32 v41, vcc, 0, v49, vcc
	global_load_dwordx4 v[40:43], v[40:41], off nt
	v_add_co_u32_e32 v44, vcc, s8, v48
	s_mov_b32 s8, 0x40000
	s_nop 0
	v_addc_co_u32_e32 v45, vcc, 0, v49, vcc
	global_load_dwordx4 v[44:47], v[44:45], off nt
	v_add_co_u32_e32 v52, vcc, s8, v48
	s_mov_b32 s8, 0x50000
	s_nop 0
	v_addc_co_u32_e32 v53, vcc, 0, v49, vcc
	global_load_dwordx4 v[52:55], v[52:53], off nt
	v_add_co_u32_e32 v56, vcc, s8, v48
	s_mov_b32 s8, 0x60000
	s_nop 0
	v_addc_co_u32_e32 v57, vcc, 0, v49, vcc
	global_load_dwordx4 v[56:59], v[56:57], off nt
	v_add_co_u32_e32 v60, vcc, s8, v48
	s_mov_b32 s8, 0x70000
	s_nop 0
	v_addc_co_u32_e32 v61, vcc, 0, v49, vcc
	global_load_dwordx4 v[60:63], v[60:61], off nt
	v_add_co_u32_e32 v48, vcc, s8, v48
	v_add_u32_e32 v3, v1, v5
	s_nop 0
	v_addc_co_u32_e32 v49, vcc, 0, v49, vcc
	global_load_dwordx4 v[64:67], v[48:49], off nt
	s_add_u32 s8, s27, s5
	s_addc_u32 s9, s34, 0
	s_waitcnt vmcnt(7)
	ds_write2_b32 v3, v32, v33 offset1:1
	ds_write2_b32 v3, v34, v35 offset0:2 offset1:3
	v_add_u32_e32 v32, 0x420, v3
	s_waitcnt vmcnt(6)
	ds_write2_b32 v32, v36, v37 offset1:1
	v_add_u32_e32 v32, 0x428, v3
	ds_write2_b32 v32, v38, v39 offset1:1
	v_add_u32_e32 v32, 0x840, v3
	s_waitcnt vmcnt(5)
	ds_write2_b32 v32, v40, v41 offset1:1
	v_add_u32_e32 v32, 0x848, v3
	ds_write2_b32 v32, v42, v43 offset1:1
	v_add_u32_e32 v32, 0xc60, v3
	v_mov_b32_e32 v42, v0
	v_mov_b32_e32 v43, v0
	s_waitcnt vmcnt(4)
	ds_write2_b32 v32, v44, v45 offset1:1
	v_add_u32_e32 v32, 0xc68, v3
	ds_write2_b32 v32, v46, v47 offset1:1
	v_add_u32_e32 v32, 0x1080, v3
	s_waitcnt vmcnt(3)
	ds_write2_b32 v32, v52, v53 offset1:1
	v_add_u32_e32 v32, 0x1088, v3
	ds_write2_b32 v32, v54, v55 offset1:1
	v_add_u32_e32 v32, 0x14a0, v3
	s_waitcnt vmcnt(2)
	ds_write2_b32 v32, v56, v57 offset1:1
	v_add_u32_e32 v32, 0x14a8, v3
	ds_write2_b32 v32, v58, v59 offset1:1
	v_add_u32_e32 v32, 0x18c0, v3
	s_waitcnt vmcnt(1)
	ds_write2_b32 v32, v60, v61 offset1:1
	v_add_u32_e32 v32, 0x18c8, v3
	ds_write2_b32 v32, v62, v63 offset1:1
	v_add_u32_e32 v32, 0x1ce0, v3
	v_add_u32_e32 v3, 0x1ce8, v3
	s_waitcnt vmcnt(0)
	ds_write2_b32 v32, v64, v65 offset1:1
	ds_write2_b32 v3, v66, v67 offset1:1
	s_waitcnt lgkmcnt(0)
	ds_read2_b32 v[34:35], v50 offset1:8
	ds_read2_b32 v[36:37], v50 offset0:33 offset1:41
	ds_read2_b32 v[44:45], v50 offset0:132 offset1:140
	ds_read2_b32 v[46:47], v50 offset0:165 offset1:173
	ds_read2_b32 v[38:39], v50 offset0:66 offset1:74
	ds_read2_b32 v[40:41], v50 offset0:99 offset1:107
	s_waitcnt lgkmcnt(5)
	v_mul_f32_e32 v3, 0x42000000, v34
	s_waitcnt lgkmcnt(4)
	v_mul_f32_e32 v34, 0x42000000, v36
	v_med3_f32 v3, v3, s83, v238
	v_med3_f32 v34, v34, s83, v238
	ds_read2_b32 v[48:49], v50 offset0:198 offset1:206
	ds_read2_b32 v[52:53], v50 offset0:231 offset1:239
	v_cvt_pk_fp8_f32 v42, v3, v34
	s_waitcnt lgkmcnt(5)
	v_mul_f32_e32 v3, 0x42000000, v44
	s_waitcnt lgkmcnt(4)
	v_mul_f32_e32 v34, 0x42000000, v46
	v_med3_f32 v3, v3, s83, v238
	v_med3_f32 v34, v34, s83, v238
	s_waitcnt lgkmcnt(3)
	v_mul_f32_e32 v36, 0x42000000, v38
	s_waitcnt lgkmcnt(2)
	v_mul_f32_e32 v38, 0x42000000, v40
	v_cvt_pk_fp8_f32 v43, v3, v34
	v_mul_f32_e32 v3, 0x42000000, v35
	v_mul_f32_e32 v34, 0x42000000, v37
	v_med3_f32 v36, v36, s83, v238
	v_med3_f32 v38, v38, s83, v238
	v_med3_f32 v3, v3, s83, v238
	v_med3_f32 v37, v34, s83, v238
	v_mov_b32_e32 v34, v0
	v_cvt_pk_fp8_f32 v42, v36, v38 op_sel:[0,0,1]
	s_waitcnt lgkmcnt(1)
	v_mul_f32_e32 v36, 0x42000000, v48
	s_waitcnt lgkmcnt(0)
	v_mul_f32_e32 v38, 0x42000000, v52
	v_cvt_pk_fp8_f32 v34, v3, v37
	v_med3_f32 v36, v36, s83, v238
	v_med3_f32 v38, v38, s83, v238
	v_cvt_pk_fp8_f32 v43, v36, v38 op_sel:[0,0,1]
	v_mul_f32_e32 v35, 0x42000000, v39
	v_mul_f32_e32 v36, 0x42000000, v41
	v_med3_f32 v35, v35, s83, v238
	v_med3_f32 v36, v36, s83, v238
	v_cvt_pk_fp8_f32 v34, v35, v36 op_sel:[0,0,1]
	v_mul_f32_e32 v3, 0x42000000, v45
	v_mul_f32_e32 v35, 0x42000000, v47
	v_med3_f32 v3, v3, s83, v238
	v_med3_f32 v38, v35, s83, v238
	v_mov_b32_e32 v35, v0
	v_cvt_pk_fp8_f32 v35, v3, v38
	v_mul_f32_e32 v36, 0x42000000, v49
	v_mul_f32_e32 v37, 0x42000000, v53
	v_med3_f32 v36, v36, s83, v238
	v_med3_f32 v37, v37, s83, v238
	v_cvt_pk_fp8_f32 v35, v36, v37 op_sel:[0,0,1]
	v_lshl_add_u64 v[32:33], s[8:9], 0, v[6:7]
	v_lshl_add_u64 v[36:37], v[32:33], 0, v[10:11]
	ds_read2_b32 v[44:45], v50 offset0:148 offset1:156
	global_store_dwordx2 v[36:37], v[34:35], off
	ds_read2_b32 v[34:35], v50 offset0:16 offset1:24
	ds_read2_b32 v[36:37], v50 offset0:49 offset1:57
	ds_read2_b32 v[46:47], v50 offset0:181 offset1:189
	ds_read2_b32 v[38:39], v50 offset0:82 offset1:90
	ds_read2_b32 v[40:41], v50 offset0:115 offset1:123
	v_lshl_add_u64 v[54:55], v[32:33], 0, v[8:9]
	s_waitcnt lgkmcnt(4)
; #define LAS __attribute__((address_space(3)))
; #define LDS_WAIT() asm volatile("s_waitcnt lgkmcnt(0)" ::: "memory")
; __device__ __forceinline__ void p0_transpose_item8(const float* W, int ldw, int srccol0, int k0, unsigned char* dst, int K, LAS float* scr, int lane) {
;     ...
;     for (int j = 0; j < 4; ++j) { const int n = (lane >> 3) + 8 * j; const LAS float* s = scr + (8 * c) * 33 + n;
;         u32x2 o; o.x = pk4_f8(s[0 * 33] * 32.f, s[1 * 33] * 32.f, s[2 * 33] * 32.f, s[3 * 33] * 32.f); o.y = pk4_f8(s[4 * 33] * 32.f, s[5 * 33] * 32.f, s[6 * 33] * 32.f, s[7 * 33] * 32.f);
;         *(u32x2*)(dst + (size_t)n * K + k0 + 8 * c) = o; }
;     LDS_WAIT(); asm volatile("" ::: "memory");
; __device__ __forceinline__ void p0_item(KP Pk, Frame& F, int it, LAS float* scr) {
;     ...
;     if (it < 32 * TI_GU) { const int le = it / TI_GU, r = it % TI_GU, kb = r / 64, nb = r % 64, n0 = 32 * nb, j = n0 >> 8, half = (n0 >> 7) & 1, c0 = 128 * j + (n0 & 127);
;         p0_transpose_item8((half ? Pk->in[I_EU] : Pk->in[I_EG]) + (size_t)le * D * DE, DE, c0, 64 * kb, ws + WS_WGU + ((size_t)le * 2048 + n0) * D, D, scr, F.lane); return; }
	v_mul_f32_e32 v3, 0x42000000, v34
	s_waitcnt lgkmcnt(3)
	v_mul_f32_e32 v34, 0x42000000, v36
	global_store_dwordx2 v[54:55], v[42:43], off
	v_med3_f32 v3, v3, s83, v238
	v_med3_f32 v34, v34, s83, v238
	v_mov_b32_e32 v42, v0
	ds_read2_b32 v[48:49], v50 offset0:214 offset1:222
	ds_read2_b32 v[52:53], v50 offset0:247 offset1:255
	v_cvt_pk_fp8_f32 v42, v3, v34
	v_mul_f32_e32 v3, 0x42000000, v44
	s_waitcnt lgkmcnt(4)
	v_mul_f32_e32 v34, 0x42000000, v46
	v_med3_f32 v3, v3, s83, v238
	v_med3_f32 v34, v34, s83, v238
	v_mov_b32_e32 v43, v0
	s_waitcnt lgkmcnt(3)
	v_mul_f32_e32 v36, 0x42000000, v38
	s_waitcnt lgkmcnt(2)
	v_mul_f32_e32 v38, 0x42000000, v40
	v_cvt_pk_fp8_f32 v43, v3, v34
	v_mul_f32_e32 v3, 0x42000000, v35
	v_mul_f32_e32 v34, 0x42000000, v37
	v_med3_f32 v36, v36, s83, v238
	v_med3_f32 v38, v38, s83, v238
	v_med3_f32 v3, v3, s83, v238
	v_med3_f32 v37, v34, s83, v238
	v_mov_b32_e32 v34, v0
	v_cvt_pk_fp8_f32 v42, v36, v38 op_sel:[0,0,1]
	s_waitcnt lgkmcnt(1)
	v_mul_f32_e32 v36, 0x42000000, v48
	s_waitcnt lgkmcnt(0)
	v_mul_f32_e32 v38, 0x42000000, v52
	v_cvt_pk_fp8_f32 v34, v3, v37
	v_med3_f32 v36, v36, s83, v238
	v_med3_f32 v38, v38, s83, v238
	v_cvt_pk_fp8_f32 v43, v36, v38 op_sel:[0,0,1]
	v_mul_f32_e32 v35, 0x42000000, v39
	v_mul_f32_e32 v36, 0x42000000, v41
	v_med3_f32 v35, v35, s83, v238
	v_med3_f32 v36, v36, s83, v238
	v_cvt_pk_fp8_f32 v34, v35, v36 op_sel:[0,0,1]
	v_mul_f32_e32 v3, 0x42000000, v45
	v_mul_f32_e32 v35, 0x42000000, v47
	v_med3_f32 v3, v3, s83, v238
	v_med3_f32 v38, v35, s83, v238
	v_mov_b32_e32 v35, v0
	v_cvt_pk_fp8_f32 v35, v3, v38
	v_mul_f32_e32 v36, 0x42000000, v49
	v_mul_f32_e32 v37, 0x42000000, v53
	v_med3_f32 v36, v36, s83, v238
	v_med3_f32 v37, v37, s83, v238
	v_cvt_pk_fp8_f32 v35, v36, v37 op_sel:[0,0,1]
	v_lshl_add_u64 v[54:55], v[32:33], 0, v[12:13]
	v_lshl_add_u64 v[32:33], v[32:33], 0, v[14:15]
	global_store_dwordx2 v[54:55], v[42:43], off
	global_store_dwordx2 v[32:33], v[34:35], off
	s_waitcnt lgkmcnt(0)
	s_mov_b64 s[8:9], 0
.LBB0_838:
	s_andn2_b64 vcc, exec, s[8:9]
	s_cbranch_vccnz .LBB0_840
	s_cmp_eq_u32 s43, 0
	s_cbranch_scc1 .Lcv_gu
	s_lshl_b32 s8, s4, 5
	s_lshl_b32 s9, s4, 4
	s_add_i32 s5, s4, 0xffffc5c0
	s_waitcnt lgkmcnt(0)
	s_and_b32 s26, s8, 0x7e0
	s_and_b32 s9, s9, 0x380
	s_and_b32 s8, s8, 0x60
	s_and_b32 s60, s5, 0xfffff800
	s_and_b32 s5, s5, 0x7c0
	s_or_b32 s27, s9, s8
	s_bitcmp0_b32 s4, 2
	s_movk_i32 s8, 0xf8
	s_cselect_b32 s8, s8, 0x100
	s_add_u32 s8, s48, s8
	s_addc_u32 s9, s49, 0
	s_load_dwordx2 s[8:9], s[8:9], 0x0
	s_lshl_b64 s[18:19], s[60:61], 12
	v_add_u32_e32 v32, s5, v2
	v_lshlrev_b32_e32 v34, 2, v4
	v_mov_b32_e32 v35, v0
	s_waitcnt lgkmcnt(0)
	s_add_u32 s18, s8, s18
	s_addc_u32 s19, s9, s19
	s_or_b32 s60, s60, s26
	s_lshl_b64 s[8:9], s[60:61], 11
	v_readlane_b32 s26, v255, 9
	s_add_u32 s26, s26, s8
	v_readlane_b32 s8, v255, 10
	s_addc_u32 s34, s8, s9
	s_lshl_b32 s8, s27, 2
	s_add_u32 s8, s18, s8
	s_addc_u32 s9, s19, 0
	v_ashrrev_i32_e32 v33, 31, v32
	v_lshl_add_u64 v[34:35], s[8:9], 0, v[34:35]
	v_lshlrev_b64 v[32:33], 12, v[32:33]
	v_lshl_add_u64 v[48:49], v[34:35], 0, v[32:33]
	s_mov_b32 s8, 0x8000
	v_add_co_u32_e32 v36, vcc, s8, v48
	global_load_dwordx4 v[32:35], v[48:49], off nt
	s_nop 0
	v_addc_co_u32_e32 v37, vcc, 0, v49, vcc
	s_mov_b32 s8, 0x10000
	global_load_dwordx4 v[36:39], v[36:37], off nt
	v_add_co_u32_e32 v40, vcc, s8, v48
	s_mov_b32 s8, 0x18000
	s_nop 0
	v_addc_co_u32_e32 v41, vcc, 0, v49, vcc
	global_load_dwordx4 v[40:43], v[40:41], off nt
	v_add_co_u32_e32 v44, vcc, s8, v48
	s_mov_b32 s8, 0x20000
	s_nop 0
	v_addc_co_u32_e32 v45, vcc, 0, v49, vcc
	global_load_dwordx4 v[44:47], v[44:45], off nt
	v_add_co_u32_e32 v52, vcc, s8, v48
	s_mov_b32 s8, 0x28000
	s_nop 0
	v_addc_co_u32_e32 v53, vcc, 0, v49, vcc
	global_load_dwordx4 v[52:55], v[52:53], off nt
	v_add_co_u32_e32 v56, vcc, s8, v48
	s_mov_b32 s8, 0x30000
	s_nop 0
	v_addc_co_u32_e32 v57, vcc, 0, v49, vcc
	global_load_dwordx4 v[56:59], v[56:57], off nt
	v_add_co_u32_e32 v60, vcc, s8, v48
	s_mov_b32 s8, 0x38000
	s_nop 0
	v_addc_co_u32_e32 v61, vcc, 0, v49, vcc
	global_load_dwordx4 v[60:63], v[60:61], off nt
	v_add_co_u32_e32 v48, vcc, s8, v48
	v_add_u32_e32 v3, v1, v5
	s_nop 0
	v_addc_co_u32_e32 v49, vcc, 0, v49, vcc
	global_load_dwordx4 v[64:67], v[48:49], off nt
	s_add_u32 s8, s26, s5
	s_addc_u32 s9, s34, 0
	s_waitcnt vmcnt(7)
	ds_write2_b32 v3, v32, v33 offset1:1
	ds_write2_b32 v3, v34, v35 offset0:2 offset1:3
	v_add_u32_e32 v32, 0x420, v3
	s_waitcnt vmcnt(6)
	ds_write2_b32 v32, v36, v37 offset1:1
	v_add_u32_e32 v32, 0x428, v3
	ds_write2_b32 v32, v38, v39 offset1:1
	v_add_u32_e32 v32, 0x840, v3
	s_waitcnt vmcnt(5)
	ds_write2_b32 v32, v40, v41 offset1:1
	v_add_u32_e32 v32, 0x848, v3
	ds_write2_b32 v32, v42, v43 offset1:1
	v_add_u32_e32 v32, 0xc60, v3
	v_mov_b32_e32 v42, v0
	v_mov_b32_e32 v43, v0
	s_waitcnt vmcnt(4)
	ds_write2_b32 v32, v44, v45 offset1:1
	v_add_u32_e32 v32, 0xc68, v3
	ds_write2_b32 v32, v46, v47 offset1:1
	v_add_u32_e32 v32, 0x1080, v3
	s_waitcnt vmcnt(3)
; #define LAS __attribute__((address_space(3)))
; #define LDS_WAIT() asm volatile("s_waitcnt lgkmcnt(0)" ::: "memory")
; __device__ __forceinline__ void p0_transpose_item8(const float* W, int ldw, int srccol0, int k0, unsigned char* dst, int K, LAS float* scr, int lane) {
;     { f32x4 v[8];
; #pragma unroll
;       for (int i = 0; i < 8; ++i) v[i] = *(const f32x4*)(W + (size_t)(k0 + 8 * i + (lane >> 3)) * ldw + srccol0 + 4 * (lane & 7));
; #pragma unroll
;       for (int i = 0; i < 8; ++i) { LAS float* p = scr + (8 * i + (lane >> 3)) * 33 + 4 * (lane & 7); p[0] = v[i][0]; p[1] = v[i][1]; p[2] = v[i][2]; p[3] = v[i][3]; } }
;     LDS_WAIT(); asm volatile("" ::: "memory");
;     const int c = lane & 7;
; #pragma unroll
;     for (int j = 0; j < 4; ++j) { const int n = (lane >> 3) + 8 * j; const LAS float* s = scr + (8 * c) * 33 + n;
;         u32x2 o; o.x = pk4_f8(s[0 * 33] * 32.f, s[1 * 33] * 32.f, s[2 * 33] * 32.f, s[3 * 33] * 32.f); o.y = pk4_f8(s[4 * 33] * 32.f, s[5 * 33] * 32.f, s[6 * 33] * 32.f, s[7 * 33] * 32.f);
;         *(u32x2*)(dst + (size_t)n * K + k0 + 8 * c) = o; }
;     LDS_WAIT(); asm volatile("" ::: "memory");
	ds_write2_b32 v32, v52, v53 offset1:1
	v_add_u32_e32 v32, 0x1088, v3
	ds_write2_b32 v32, v54, v55 offset1:1
	v_add_u32_e32 v32, 0x14a0, v3
	s_waitcnt vmcnt(2)
	ds_write2_b32 v32, v56, v57 offset1:1
	v_add_u32_e32 v32, 0x14a8, v3
	ds_write2_b32 v32, v58, v59 offset1:1
	v_add_u32_e32 v32, 0x18c0, v3
	s_waitcnt vmcnt(1)
	ds_write2_b32 v32, v60, v61 offset1:1
	v_add_u32_e32 v32, 0x18c8, v3
	ds_write2_b32 v32, v62, v63 offset1:1
	v_add_u32_e32 v32, 0x1ce0, v3
	v_add_u32_e32 v3, 0x1ce8, v3
	s_waitcnt vmcnt(0)
	ds_write2_b32 v32, v64, v65 offset1:1
	ds_write2_b32 v3, v66, v67 offset1:1
	s_waitcnt lgkmcnt(0)
	ds_read2_b32 v[34:35], v50 offset1:8
	ds_read2_b32 v[36:37], v50 offset0:33 offset1:41
	ds_read2_b32 v[44:45], v50 offset0:132 offset1:140
	ds_read2_b32 v[46:47], v50 offset0:165 offset1:173
	ds_read2_b32 v[38:39], v50 offset0:66 offset1:74
	ds_read2_b32 v[40:41], v50 offset0:99 offset1:107
	s_waitcnt lgkmcnt(5)
	v_mul_f32_e32 v3, 0x42000000, v34
	s_waitcnt lgkmcnt(4)
	v_mul_f32_e32 v34, 0x42000000, v36
	v_med3_f32 v3, v3, s83, v238
	v_med3_f32 v34, v34, s83, v238
	ds_read2_b32 v[48:49], v50 offset0:198 offset1:206
	ds_read2_b32 v[52:53], v50 offset0:231 offset1:239
	v_cvt_pk_fp8_f32 v42, v3, v34
	s_waitcnt lgkmcnt(5)
	v_mul_f32_e32 v3, 0x42000000, v44
	s_waitcnt lgkmcnt(4)
	v_mul_f32_e32 v34, 0x42000000, v46
	v_med3_f32 v3, v3, s83, v238
	v_med3_f32 v34, v34, s83, v238
	s_waitcnt lgkmcnt(3)
	v_mul_f32_e32 v36, 0x42000000, v38
	s_waitcnt lgkmcnt(2)
	v_mul_f32_e32 v38, 0x42000000, v40
	v_cvt_pk_fp8_f32 v43, v3, v34
	v_mul_f32_e32 v3, 0x42000000, v35
	v_mul_f32_e32 v34, 0x42000000, v37
	v_med3_f32 v36, v36, s83, v238
	v_med3_f32 v38, v38, s83, v238
	v_med3_f32 v3, v3, s83, v238
	v_med3_f32 v37, v34, s83, v238
	v_mov_b32_e32 v34, v0
	v_cvt_pk_fp8_f32 v42, v36, v38 op_sel:[0,0,1]
	s_waitcnt lgkmcnt(1)
	v_mul_f32_e32 v36, 0x42000000, v48
	s_waitcnt lgkmcnt(0)
	v_mul_f32_e32 v38, 0x42000000, v52
	v_cvt_pk_fp8_f32 v34, v3, v37
	v_med3_f32 v36, v36, s83, v238
	v_med3_f32 v38, v38, s83, v238
	v_cvt_pk_fp8_f32 v43, v36, v38 op_sel:[0,0,1]
	v_mul_f32_e32 v35, 0x42000000, v39
	v_mul_f32_e32 v36, 0x42000000, v41
	v_med3_f32 v35, v35, s83, v238
	v_med3_f32 v36, v36, s83, v238
	v_cvt_pk_fp8_f32 v34, v35, v36 op_sel:[0,0,1]
	v_mul_f32_e32 v3, 0x42000000, v45
	v_mul_f32_e32 v35, 0x42000000, v47
	v_med3_f32 v3, v3, s83, v238
	v_med3_f32 v38, v35, s83, v238
	v_mov_b32_e32 v35, v0
	v_cvt_pk_fp8_f32 v35, v3, v38
	v_mul_f32_e32 v36, 0x42000000, v49
	v_mul_f32_e32 v37, 0x42000000, v53
	v_med3_f32 v36, v36, s83, v238
	v_med3_f32 v37, v37, s83, v238
	v_cvt_pk_fp8_f32 v35, v36, v37 op_sel:[0,0,1]
	v_lshl_add_u64 v[32:33], s[8:9], 0, v[6:7]
	v_lshl_add_u64 v[36:37], v[32:33], 0, v[18:19]
	ds_read2_b32 v[44:45], v50 offset0:148 offset1:156
	global_store_dwordx2 v[36:37], v[34:35], off
	ds_read2_b32 v[34:35], v50 offset0:16 offset1:24
	ds_read2_b32 v[36:37], v50 offset0:49 offset1:57
	ds_read2_b32 v[46:47], v50 offset0:181 offset1:189
	ds_read2_b32 v[38:39], v50 offset0:82 offset1:90
	ds_read2_b32 v[40:41], v50 offset0:115 offset1:123
	v_lshl_add_u64 v[54:55], v[32:33], 0, v[16:17]
	s_waitcnt lgkmcnt(4)
	v_mul_f32_e32 v3, 0x42000000, v34
	s_waitcnt lgkmcnt(3)
	v_mul_f32_e32 v34, 0x42000000, v36
	global_store_dwordx2 v[54:55], v[42:43], off
	v_med3_f32 v3, v3, s83, v238
	v_med3_f32 v34, v34, s83, v238
	v_mov_b32_e32 v42, v0
	ds_read2_b32 v[48:49], v50 offset0:214 offset1:222
	ds_read2_b32 v[52:53], v50 offset0:247 offset1:255
	v_cvt_pk_fp8_f32 v42, v3, v34
	v_mul_f32_e32 v3, 0x42000000, v44
	s_waitcnt lgkmcnt(4)
	v_mul_f32_e32 v34, 0x42000000, v46
	v_med3_f32 v3, v3, s83, v238
	v_med3_f32 v34, v34, s83, v238
	v_mov_b32_e32 v43, v0
	s_waitcnt lgkmcnt(3)
	v_mul_f32_e32 v36, 0x42000000, v38
	s_waitcnt lgkmcnt(2)
	v_mul_f32_e32 v38, 0x42000000, v40
	v_cvt_pk_fp8_f32 v43, v3, v34
	v_mul_f32_e32 v3, 0x42000000, v35
	v_mul_f32_e32 v34, 0x42000000, v37
	v_med3_f32 v36, v36, s83, v238
	v_med3_f32 v38, v38, s83, v238
	v_med3_f32 v3, v3, s83, v238
	v_med3_f32 v37, v34, s83, v238
	v_mov_b32_e32 v34, v0
	v_cvt_pk_fp8_f32 v42, v36, v38 op_sel:[0,0,1]
	s_waitcnt lgkmcnt(1)
	v_mul_f32_e32 v36, 0x42000000, v48
	s_waitcnt lgkmcnt(0)
	v_mul_f32_e32 v38, 0x42000000, v52
	v_cvt_pk_fp8_f32 v34, v3, v37
	v_med3_f32 v36, v36, s83, v238
	v_med3_f32 v38, v38, s83, v238
	v_cvt_pk_fp8_f32 v43, v36, v38 op_sel:[0,0,1]
	v_mul_f32_e32 v35, 0x42000000, v39
	v_mul_f32_e32 v36, 0x42000000, v41
	v_med3_f32 v35, v35, s83, v238
	v_med3_f32 v36, v36, s83, v238
	v_cvt_pk_fp8_f32 v34, v35, v36 op_sel:[0,0,1]
	v_mul_f32_e32 v3, 0x42000000, v45
	v_mul_f32_e32 v35, 0x42000000, v47
	v_med3_f32 v3, v3, s83, v238
	v_med3_f32 v38, v35, s83, v238
	v_mov_b32_e32 v35, v0
	v_cvt_pk_fp8_f32 v35, v3, v38
	v_mul_f32_e32 v36, 0x42000000, v49
	v_mul_f32_e32 v37, 0x42000000, v53
	v_med3_f32 v36, v36, s83, v238
	v_med3_f32 v37, v37, s83, v238
	v_cvt_pk_fp8_f32 v35, v36, v37 op_sel:[0,0,1]
	v_lshl_add_u64 v[54:55], v[32:33], 0, v[20:21]
	v_lshl_add_u64 v[32:33], v[32:33], 0, v[22:23]
	global_store_dwordx2 v[54:55], v[42:43], off
	global_store_dwordx2 v[32:33], v[34:35], off
	s_waitcnt lgkmcnt(0)

; #define LAS __attribute__((address_space(3)))
; #define LDS_WAIT() asm volatile("s_waitcnt lgkmcnt(0)" ::: "memory")
; __device__ __forceinline__ void p0_transpose_item8(const float* W, int ldw, int srccol0, int k0, unsigned char* dst, int K, LAS float* scr, int lane) {
;     { f32x4 v[8];
; #pragma unroll
;       for (int i = 0; i < 8; ++i) v[i] = *(const f32x4*)(W + (size_t)(k0 + 8 * i + (lane >> 3)) * ldw + srccol0 + 4 * (lane & 7));
; #pragma unroll
;       for (int i = 0; i < 8; ++i) { LAS float* p = scr + (8 * i + (lane >> 3)) * 33 + 4 * (lane & 7); p[0] = v[i][0]; p[1] = v[i][1]; p[2] = v[i][2]; p[3] = v[i][3]; } }
;     LDS_WAIT(); asm volatile("" ::: "memory");
;     const int c = lane & 7;
; #pragma unroll
;     for (int j = 0; j < 4; ++j) { const int n = (lane >> 3) + 8 * j; const LAS float* s = scr + (8 * c) * 33 + n;
;         u32x2 o; o.x = pk4_f8(s[0 * 33] * 32.f, s[1 * 33] * 32.f, s[2 * 33] * 32.f, s[3 * 33] * 32.f); o.y = pk4_f8(s[4 * 33] * 32.f, s[5 * 33] * 32.f, s[6 * 33] * 32.f, s[7 * 33] * 32.f);
;         *(u32x2*)(dst + (size_t)n * K + k0 + 8 * c) = o; }
;     LDS_WAIT(); asm volatile("" ::: "memory");
; __device__ __forceinline__ void p0_item(KP Pk, Frame& F, int it, LAS float* scr) {
;     ...
;         { const int kb = r / 64, nb = r % 64;
;           if (WOUT_F8) p0_transpose_item8(Pk->in[I_WOUT] + (size_t)l * D * D, D, 32 * nb, 64 * kb, ws + WS_WOUT + ((size_t)l * D + 32 * nb) * D, D, scr, F.lane);
;           else p0_transpose_item(Pk->in[I_WOUT] + (size_t)l * D * D, D, 32 * nb, 64 * kb, (bf16_t*)(ws + WS_WOUT) + ((size_t)l * D + 32 * nb) * D, D, scr, F.lane); return; }
.LBB0_841:
	s_mul_hi_i32 s5, s4, 0x8ca29c05
	s_add_i32 s5, s5, s4
	s_lshr_b32 s8, s5, 31
	s_ashr_i32 s5, s5, 12
	s_add_i32 s60, s5, s8
	s_mul_i32 s5, s60, 0x1d20
	s_sub_i32 s4, s4, s5
	s_cmpk_gt_i32 s4, 0x14ff
	s_mov_b64 s[8:9], -1
	s_cbranch_scc0 .LBB0_850
	s_cmpk_gt_u32 s4, 0x151f
	s_cbranch_scc0 .LBB0_844
	s_load_dwordx2 s[8:9], s[48:49], 0x48
	s_add_i32 s5, s4, 0xffffeae0
	s_ashr_i32 s19, s60, 31
	s_mov_b32 s18, s60
	s_and_b32 s34, s5, 0xffffffc0
	s_waitcnt lgkmcnt(0)
	s_lshl_b64 s[26:27], s[18:19], 24
	s_waitcnt lgkmcnt(0)
	s_add_u32 s26, s8, s26
	s_addc_u32 s27, s9, s27
	s_lshl_b32 s5, s5, 5
	s_and_b32 s5, s5, 0x7e0
	s_lshl_b64 s[8:9], s[18:19], 22
	s_lshl_b32 s18, s5, 11
	v_readlane_b32 s19, v255, 11
	s_add_u32 s8, s19, s8
	v_readlane_b32 s19, v255, 12
	s_addc_u32 s9, s19, s9
	s_add_u32 s18, s8, s18
	s_addc_u32 s19, s9, 0
	s_lshl_b32 s5, s5, 2
	v_add_u32_e32 v32, s34, v2
	s_add_u32 s8, s26, s5
	s_addc_u32 s9, s27, 0
	v_lshlrev_b32_e32 v34, 2, v4
	v_mov_b32_e32 v35, v0
	v_ashrrev_i32_e32 v33, 31, v32
	v_lshl_add_u64 v[34:35], s[8:9], 0, v[34:35]
	v_lshlrev_b64 v[32:33], 13, v[32:33]
	v_lshl_add_u64 v[48:49], v[34:35], 0, v[32:33]
	s_mov_b32 s5, 0x10000
	v_add_co_u32_e32 v36, vcc, s5, v48
	global_load_dwordx4 v[32:35], v[48:49], off nt
	s_nop 0
	v_addc_co_u32_e32 v37, vcc, 0, v49, vcc
	s_mov_b32 s5, 0x20000
	global_load_dwordx4 v[36:39], v[36:37], off nt
	v_add_co_u32_e32 v40, vcc, s5, v48
	s_mov_b32 s5, 0x30000
	s_nop 0
	v_addc_co_u32_e32 v41, vcc, 0, v49, vcc
	global_load_dwordx4 v[40:43], v[40:41], off nt
	v_add_co_u32_e32 v44, vcc, s5, v48
	s_mov_b32 s5, 0x40000
	s_nop 0
	v_addc_co_u32_e32 v45, vcc, 0, v49, vcc
	global_load_dwordx4 v[44:47], v[44:45], off nt
	v_add_co_u32_e32 v52, vcc, s5, v48
	s_mov_b32 s5, 0x50000
	s_nop 0
	v_addc_co_u32_e32 v53, vcc, 0, v49, vcc
	global_load_dwordx4 v[52:55], v[52:53], off nt
	v_add_co_u32_e32 v56, vcc, s5, v48
	s_mov_b32 s5, 0x60000
	s_nop 0
	v_addc_co_u32_e32 v57, vcc, 0, v49, vcc
	global_load_dwordx4 v[56:59], v[56:57], off nt
	v_add_co_u32_e32 v60, vcc, s5, v48
	s_mov_b32 s5, 0x70000
	s_nop 0
	v_addc_co_u32_e32 v61, vcc, 0, v49, vcc
	global_load_dwordx4 v[60:63], v[60:61], off nt
	v_add_co_u32_e32 v48, vcc, s5, v48
	v_add_u32_e32 v3, v1, v5
	s_nop 0
	v_addc_co_u32_e32 v49, vcc, 0, v49, vcc
	global_load_dwordx4 v[64:67], v[48:49], off nt
	s_add_u32 s8, s18, s34
	s_addc_u32 s9, s19, 0
	s_waitcnt vmcnt(7)
	ds_write2_b32 v3, v32, v33 offset1:1
	ds_write2_b32 v3, v34, v35 offset0:2 offset1:3
	v_add_u32_e32 v32, 0x420, v3
	s_waitcnt vmcnt(6)
	ds_write2_b32 v32, v36, v37 offset1:1
	v_add_u32_e32 v32, 0x428, v3
	ds_write2_b32 v32, v38, v39 offset1:1
	v_add_u32_e32 v32, 0x840, v3
	s_waitcnt vmcnt(5)
	ds_write2_b32 v32, v40, v41 offset1:1
	v_add_u32_e32 v32, 0x848, v3
	ds_write2_b32 v32, v42, v43 offset1:1
	v_add_u32_e32 v32, 0xc60, v3
	v_mov_b32_e32 v42, v0
	v_mov_b32_e32 v43, v0
	s_waitcnt vmcnt(4)
	ds_write2_b32 v32, v44, v45 offset1:1
	v_add_u32_e32 v32, 0xc68, v3
	ds_write2_b32 v32, v46, v47 offset1:1
	v_add_u32_e32 v32, 0x1080, v3
	s_waitcnt vmcnt(3)
	ds_write2_b32 v32, v52, v53 offset1:1
	v_add_u32_e32 v32, 0x1088, v3
	ds_write2_b32 v32, v54, v55 offset1:1
	v_add_u32_e32 v32, 0x14a0, v3
	s_waitcnt vmcnt(2)
	ds_write2_b32 v32, v56, v57 offset1:1
	v_add_u32_e32 v32, 0x14a8, v3
	ds_write2_b32 v32, v58, v59 offset1:1
	v_add_u32_e32 v32, 0x18c0, v3
	s_waitcnt vmcnt(1)
	ds_write2_b32 v32, v60, v61 offset1:1
	v_add_u32_e32 v32, 0x18c8, v3
	ds_write2_b32 v32, v62, v63 offset1:1
	v_add_u32_e32 v32, 0x1ce0, v3
	v_add_u32_e32 v3, 0x1ce8, v3
	s_waitcnt vmcnt(0)
	ds_write2_b32 v32, v64, v65 offset1:1
	ds_write2_b32 v3, v66, v67 offset1:1
	s_waitcnt lgkmcnt(0)
	ds_read2_b32 v[34:35], v50 offset1:8
	ds_read2_b32 v[36:37], v50 offset0:33 offset1:41
	ds_read2_b32 v[44:45], v50 offset0:132 offset1:140
	ds_read2_b32 v[46:47], v50 offset0:165 offset1:173
	ds_read2_b32 v[38:39], v50 offset0:66 offset1:74
	ds_read2_b32 v[40:41], v50 offset0:99 offset1:107
	s_waitcnt lgkmcnt(5)
	v_mul_f32_e32 v3, 0x42000000, v34
	s_waitcnt lgkmcnt(4)
	v_mul_f32_e32 v34, 0x42000000, v36
	v_med3_f32 v3, v3, s83, v238
	v_med3_f32 v34, v34, s83, v238
	ds_read2_b32 v[48:49], v50 offset0:198 offset1:206
	ds_read2_b32 v[52:53], v50 offset0:231 offset1:239
	v_cvt_pk_fp8_f32 v42, v3, v34
	s_waitcnt lgkmcnt(5)
	v_mul_f32_e32 v3, 0x42000000, v44
	s_waitcnt lgkmcnt(4)
	v_mul_f32_e32 v34, 0x42000000, v46
	v_med3_f32 v3, v3, s83, v238
	v_med3_f32 v34, v34, s83, v238
	s_waitcnt lgkmcnt(3)
	v_mul_f32_e32 v36, 0x42000000, v38
	s_waitcnt lgkmcnt(2)
	v_mul_f32_e32 v38, 0x42000000, v40
	v_cvt_pk_fp8_f32 v43, v3, v34
	v_mul_f32_e32 v3, 0x42000000, v35
	v_mul_f32_e32 v34, 0x42000000, v37
	v_med3_f32 v36, v36, s83, v238
	v_med3_f32 v38, v38, s83, v238
	v_med3_f32 v3, v3, s83, v238
	v_med3_f32 v37, v34, s83, v238
	v_mov_b32_e32 v34, v0
	v_cvt_pk_fp8_f32 v42, v36, v38 op_sel:[0,0,1]
	s_waitcnt lgkmcnt(1)
	v_mul_f32_e32 v36, 0x42000000, v48
	s_waitcnt lgkmcnt(0)
	v_mul_f32_e32 v38, 0x42000000, v52
	v_cvt_pk_fp8_f32 v34, v3, v37
	v_med3_f32 v36, v36, s83, v238
	v_med3_f32 v38, v38, s83, v238
	v_cvt_pk_fp8_f32 v43, v36, v38 op_sel:[0,0,1]
	v_mul_f32_e32 v35, 0x42000000, v39
	v_mul_f32_e32 v36, 0x42000000, v41
	v_med3_f32 v35, v35, s83, v238
	v_med3_f32 v36, v36, s83, v238
	v_cvt_pk_fp8_f32 v34, v35, v36 op_sel:[0,0,1]
	v_mul_f32_e32 v3, 0x42000000, v45
	v_mul_f32_e32 v35, 0x42000000, v47
	v_med3_f32 v3, v3, s83, v238
	v_med3_f32 v38, v35, s83, v238
	v_mov_b32_e32 v35, v0
	v_cvt_pk_fp8_f32 v35, v3, v38
	v_mul_f32_e32 v36, 0x42000000, v49
	v_mul_f32_e32 v37, 0x42000000, v53
	v_med3_f32 v36, v36, s83, v238
	v_med3_f32 v37, v37, s83, v238
	v_cvt_pk_fp8_f32 v35, v36, v37 op_sel:[0,0,1]
	v_lshl_add_u64 v[32:33], s[8:9], 0, v[6:7]
	v_lshl_add_u64 v[36:37], v[32:33], 0, v[18:19]
	ds_read2_b32 v[44:45], v50 offset0:148 offset1:156
	global_store_dwordx2 v[36:37], v[34:35], off
	ds_read2_b32 v[34:35], v50 offset0:16 offset1:24
	ds_read2_b32 v[36:37], v50 offset0:49 offset1:57
	ds_read2_b32 v[46:47], v50 offset0:181 offset1:189
	ds_read2_b32 v[38:39], v50 offset0:82 offset1:90
	ds_read2_b32 v[40:41], v50 offset0:115 offset1:123
	v_lshl_add_u64 v[54:55], v[32:33], 0, v[16:17]
	s_waitcnt lgkmcnt(4)
; #define LAS __attribute__((address_space(3)))
; #define LDS_WAIT() asm volatile("s_waitcnt lgkmcnt(0)" ::: "memory")
; __device__ __forceinline__ void p0_transpose_item8(const float* W, int ldw, int srccol0, int k0, unsigned char* dst, int K, LAS float* scr, int lane) {
;     ...
;     for (int j = 0; j < 4; ++j) { const int n = (lane >> 3) + 8 * j; const LAS float* s = scr + (8 * c) * 33 + n;
;         u32x2 o; o.x = pk4_f8(s[0 * 33] * 32.f, s[1 * 33] * 32.f, s[2 * 33] * 32.f, s[3 * 33] * 32.f); o.y = pk4_f8(s[4 * 33] * 32.f, s[5 * 33] * 32.f, s[6 * 33] * 32.f, s[7 * 33] * 32.f);
;         *(u32x2*)(dst + (size_t)n * K + k0 + 8 * c) = o; }
;     LDS_WAIT(); asm volatile("" ::: "memory");
; __device__ __forceinline__ void p0_item(KP Pk, Frame& F, int it, LAS float* scr) {
;     ...
;         if (r < TI_WA) { if (WIN_F8_L(l)) p0_transpose_item8(Pk->in[I_WIN] + (size_t)l * D * DIN, DIN, 1536, 64 * r, ws + WS_WA + (size_t)l * 32 * D * 2, D, scr, F.lane);
;             else p0_transpose_item(Pk->in[I_WIN] + (size_t)l * D * DIN, DIN, 1536, 64 * r, (bf16_t*)(ws + WS_WA) + (size_t)l * 32 * D, D, scr, F.lane); return; }
	v_mul_f32_e32 v3, 0x42000000, v34
	s_waitcnt lgkmcnt(3)
	v_mul_f32_e32 v34, 0x42000000, v36
	global_store_dwordx2 v[54:55], v[42:43], off
	v_med3_f32 v3, v3, s83, v238
	v_med3_f32 v34, v34, s83, v238
	v_mov_b32_e32 v42, v0
	ds_read2_b32 v[48:49], v50 offset0:214 offset1:222
	ds_read2_b32 v[52:53], v50 offset0:247 offset1:255
	v_cvt_pk_fp8_f32 v42, v3, v34
	v_mul_f32_e32 v3, 0x42000000, v44
	s_waitcnt lgkmcnt(4)
	v_mul_f32_e32 v34, 0x42000000, v46
	v_med3_f32 v3, v3, s83, v238
	v_med3_f32 v34, v34, s83, v238
	v_mov_b32_e32 v43, v0
	s_waitcnt lgkmcnt(3)
	v_mul_f32_e32 v36, 0x42000000, v38
	s_waitcnt lgkmcnt(2)
	v_mul_f32_e32 v38, 0x42000000, v40
	v_cvt_pk_fp8_f32 v43, v3, v34
	v_mul_f32_e32 v3, 0x42000000, v35
	v_mul_f32_e32 v34, 0x42000000, v37
	v_med3_f32 v36, v36, s83, v238
	v_med3_f32 v38, v38, s83, v238
	v_med3_f32 v3, v3, s83, v238
	v_med3_f32 v37, v34, s83, v238
	v_mov_b32_e32 v34, v0
	v_cvt_pk_fp8_f32 v42, v36, v38 op_sel:[0,0,1]
	s_waitcnt lgkmcnt(1)
	v_mul_f32_e32 v36, 0x42000000, v48
	s_waitcnt lgkmcnt(0)
	v_mul_f32_e32 v38, 0x42000000, v52
	v_cvt_pk_fp8_f32 v34, v3, v37
	v_med3_f32 v36, v36, s83, v238
	v_med3_f32 v38, v38, s83, v238
	v_cvt_pk_fp8_f32 v43, v36, v38 op_sel:[0,0,1]
	v_mul_f32_e32 v35, 0x42000000, v39
	v_mul_f32_e32 v36, 0x42000000, v41
	v_med3_f32 v35, v35, s83, v238
	v_med3_f32 v36, v36, s83, v238
	v_cvt_pk_fp8_f32 v34, v35, v36 op_sel:[0,0,1]
	v_mul_f32_e32 v3, 0x42000000, v45
	v_mul_f32_e32 v35, 0x42000000, v47
	v_med3_f32 v3, v3, s83, v238
	v_med3_f32 v38, v35, s83, v238
	v_mov_b32_e32 v35, v0
	v_cvt_pk_fp8_f32 v35, v3, v38
	v_mul_f32_e32 v36, 0x42000000, v49
	v_mul_f32_e32 v37, 0x42000000, v53
	v_med3_f32 v36, v36, s83, v238
	v_med3_f32 v37, v37, s83, v238
	v_cvt_pk_fp8_f32 v35, v36, v37 op_sel:[0,0,1]
	v_lshl_add_u64 v[54:55], v[32:33], 0, v[20:21]
	v_lshl_add_u64 v[32:33], v[32:33], 0, v[22:23]
	global_store_dwordx2 v[54:55], v[42:43], off
	global_store_dwordx2 v[32:33], v[34:35], off
	s_waitcnt lgkmcnt(0)
	s_mov_b64 s[8:9], 0
.LBB0_844:
	s_andn2_b64 vcc, exec, s[8:9]
	s_cbranch_vccnz .LBB0_849
	s_lshl_b32 s5, s4, 6
	s_add_i32 s8, s5, 0xfffac000
	s_waitcnt lgkmcnt(0)
	s_load_dwordx2 s[26:27], s[48:49], 0x40
	v_add_u32_e32 v3, s8, v2
	v_add_u32_e32 v32, 8, v3
	v_mad_i64_i32 v[34:35], s[18:19], v32, s2, 0
	v_add_u32_e32 v32, 16, v3
	s_cmp_gt_u32 s60, 1
	v_mad_i64_i32 v[36:37], s[18:19], v3, s2, 0
	v_mad_i64_i32 v[32:33], s[18:19], v32, s2, 0
	s_mov_b64 s[34:35], -1
	v_add_u32_e32 v41, 24, v3
	v_add_u32_e32 v40, 32, v3
	v_add_u32_e32 v39, 40, v3
	v_add_u32_e32 v38, 48, v3
	v_add_u32_e32 v3, 56, v3
	s_cbranch_scc1 .LBB0_847
	s_mul_i32 s9, s60, 0x2a40000
	s_mul_hi_u32 s5, s60, 0x2a40000
	s_waitcnt lgkmcnt(0)
	s_add_u32 s18, s26, s9
	s_addc_u32 s19, s27, s5
	v_lshlrev_b32_e32 v42, 2, v4
	v_mov_b32_e32 v43, v0
	v_lshl_add_u64 v[42:43], s[18:19], 0, v[42:43]
	s_mov_b64 s[18:19], 0x1800
	v_lshl_add_u64 v[72:73], v[42:43], 0, s[18:19]
	v_lshl_add_u64 v[42:43], v[72:73], 0, v[36:37]
	v_lshl_add_u64 v[46:47], v[72:73], 0, v[34:35]
	v_lshl_add_u64 v[52:53], v[72:73], 0, v[32:33]
	v_mad_i64_i32 v[56:57], s[18:19], v41, s2, v[72:73]
	v_mad_i64_i32 v[60:61], s[18:19], v40, s2, v[72:73]
	v_mad_i64_i32 v[64:65], s[18:19], v39, s2, v[72:73]
	global_load_dwordx4 v[42:45], v[42:43], off nt
	s_nop 0
	global_load_dwordx4 v[46:49], v[46:47], off nt
	s_nop 0
	global_load_dwordx4 v[52:55], v[52:53], off nt
	s_nop 0
	global_load_dwordx4 v[56:59], v[56:57], off nt
	s_nop 0
	global_load_dwordx4 v[60:63], v[60:61], off nt
	s_nop 0
	global_load_dwordx4 v[64:67], v[64:65], off nt
	v_mad_i64_i32 v[68:69], s[18:19], v38, s2, v[72:73]
	global_load_dwordx4 v[68:71], v[68:69], off nt
	v_mad_i64_i32 v[72:73], s[18:19], v3, s2, v[72:73]
	global_load_dwordx4 v[72:75], v[72:73], off nt
	v_add_u32_e32 v51, v1, v5
	v_add_u32_e32 v82, 0x420, v51
	v_add_u32_e32 v83, 0x428, v51
	v_add_u32_e32 v84, 0x840, v51
	v_add_u32_e32 v85, 0x848, v51
	v_add_u32_e32 v86, 0xc60, v51
	v_add_u32_e32 v87, 0xc68, v51
	v_add_u32_e32 v88, 0x1080, v51
	v_add_u32_e32 v89, 0x1088, v51
	v_add_u32_e32 v90, 0x14a0, v51
	v_add_u32_e32 v91, 0x14a8, v51
	v_add_u32_e32 v92, 0x18c0, v51
	v_add_u32_e32 v93, 0x18c8, v51
	v_add_u32_e32 v94, 0x1ce0, v51
	v_add_u32_e32 v95, 0x1ce8, v51
	v_mov_b32_e32 v77, v0
	v_mov_b32_e32 v76, v0
	s_lshl_b64 s[18:19], s[60:61], 17
	v_readlane_b32 s5, v255, 13
	s_add_u32 s5, s5, s18
	v_readlane_b32 s9, v255, 14
	s_addc_u32 s9, s9, s19
	s_add_u32 s18, s5, s8
	s_addc_u32 s19, s9, 0
	v_lshl_add_u64 v[78:79], s[18:19], 0, v[6:7]
	v_lshl_add_u64 v[80:81], v[78:79], 0, v[16:17]
	s_mov_b64 s[34:35], 0
	s_waitcnt vmcnt(7)
	ds_write2_b32 v51, v42, v43 offset1:1
	ds_write2_b32 v51, v44, v45 offset0:2 offset1:3
	s_waitcnt vmcnt(6)
	ds_write2_b32 v82, v46, v47 offset1:1
	ds_write2_b32 v83, v48, v49 offset1:1
	s_waitcnt vmcnt(5)
	ds_write2_b32 v84, v52, v53 offset1:1
	ds_write2_b32 v85, v54, v55 offset1:1
	s_waitcnt vmcnt(4)
	ds_write2_b32 v86, v56, v57 offset1:1
	ds_write2_b32 v87, v58, v59 offset1:1
	s_waitcnt vmcnt(3)
	ds_write2_b32 v88, v60, v61 offset1:1
	ds_write2_b32 v89, v62, v63 offset1:1
	s_waitcnt vmcnt(2)
	ds_write2_b32 v90, v64, v65 offset1:1
	ds_write2_b32 v91, v66, v67 offset1:1
	s_waitcnt vmcnt(1)
	ds_write2_b32 v92, v68, v69 offset1:1
	ds_write2_b32 v93, v70, v71 offset1:1
	s_waitcnt vmcnt(0)
	ds_write2_b32 v94, v72, v73 offset1:1
	ds_write2_b32 v95, v74, v75 offset1:1
	s_waitcnt lgkmcnt(0)
	ds_read2_b32 v[42:43], v50 offset1:8
	ds_read2_b32 v[44:45], v50 offset0:33 offset1:41
	ds_read2_b32 v[46:47], v50 offset0:66 offset1:74
	ds_read2_b32 v[48:49], v50 offset0:99 offset1:107
	ds_read2_b32 v[52:53], v50 offset0:132 offset1:140
	ds_read2_b32 v[54:55], v50 offset0:165 offset1:173
	ds_read2_b32 v[56:57], v50 offset0:198 offset1:206
	ds_read2_b32 v[58:59], v50 offset0:231 offset1:239
	s_waitcnt lgkmcnt(7)
; #define LAS __attribute__((address_space(3)))
; #define LDS_WAIT() asm volatile("s_waitcnt lgkmcnt(0)" ::: "memory")
; __device__ __forceinline__ void p0_transpose_item(const float* W, int ldw, int srccol0, int k0, bf16_t* dst, int K, LAS float* scr, int lane, bool q = false) {
;     { f32x4 v[8];
; #pragma unroll
;       for (int i = 0; i < 8; ++i) v[i] = *(const f32x4*)(W + (size_t)(k0 + 8 * i + (lane >> 3)) * ldw + srccol0 + 4 * (lane & 7));
; __device__ __forceinline__ void p0_transpose_item8(const float* W, int ldw, int srccol0, int k0, unsigned char* dst, int K, LAS float* scr, int lane) {
;     ...
;     LDS_WAIT(); asm volatile("" ::: "memory");
;     const int c = lane & 7;
; #pragma unroll
;     for (int j = 0; j < 4; ++j) { const int n = (lane >> 3) + 8 * j; const LAS float* s = scr + (8 * c) * 33 + n;
;         u32x2 o; o.x = pk4_f8(s[0 * 33] * 32.f, s[1 * 33] * 32.f, s[2 * 33] * 32.f, s[3 * 33] * 32.f); o.y = pk4_f8(s[4 * 33] * 32.f, s[5 * 33] * 32.f, s[6 * 33] * 32.f, s[7 * 33] * 32.f);
;         *(u32x2*)(dst + (size_t)n * K + k0 + 8 * c) = o; }
;     LDS_WAIT(); asm volatile("" ::: "memory");
	v_mul_f32_e32 v42, 0x42000000, v42
	s_waitcnt lgkmcnt(3)
	v_mul_f32_e32 v51, 0x42000000, v52
	s_waitcnt lgkmcnt(2)
	v_mul_f32_e32 v52, 0x42000000, v54
	v_med3_f32 v51, v51, s83, v238
	v_med3_f32 v52, v52, s83, v238
	v_cvt_pk_fp8_f32 v77, v51, v52
	v_mul_f32_e32 v44, 0x42000000, v44
	s_waitcnt lgkmcnt(1)
	v_mul_f32_e32 v54, 0x42000000, v56
	s_waitcnt lgkmcnt(0)
	v_mul_f32_e32 v56, 0x42000000, v58
	v_med3_f32 v42, v42, s83, v238
	v_med3_f32 v44, v44, s83, v238
	v_mul_f32_e32 v43, 0x42000000, v43
	v_mul_f32_e32 v45, 0x42000000, v45
	v_cvt_pk_fp8_f32 v76, v42, v44
	v_med3_f32 v42, v54, s83, v238
	v_med3_f32 v44, v56, s83, v238
	v_cvt_pk_fp8_f32 v77, v42, v44 op_sel:[0,0,1]
	v_med3_f32 v43, v43, s83, v238
	v_med3_f32 v45, v45, s83, v238
	v_mov_b32_e32 v42, v0
	v_cvt_pk_fp8_f32 v42, v43, v45
	v_mul_f32_e32 v44, 0x42000000, v47
	v_mul_f32_e32 v43, 0x42000000, v49
	v_mul_f32_e32 v46, 0x42000000, v46
	v_mul_f32_e32 v48, 0x42000000, v48
	v_med3_f32 v44, v44, s83, v238
	v_med3_f32 v43, v43, s83, v238
	v_med3_f32 v46, v46, s83, v238
	v_med3_f32 v48, v48, s83, v238
	v_cvt_pk_fp8_f32 v42, v44, v43 op_sel:[0,0,1]
	v_mul_f32_e32 v43, 0x42000000, v53
	v_mul_f32_e32 v44, 0x42000000, v55
	v_cvt_pk_fp8_f32 v76, v46, v48 op_sel:[0,0,1]
	v_med3_f32 v46, v43, s83, v238
	v_med3_f32 v44, v44, s83, v238
	v_mov_b32_e32 v43, v0
	v_cvt_pk_fp8_f32 v43, v46, v44
	v_mul_f32_e32 v45, 0x42000000, v57
	v_mul_f32_e32 v44, 0x42000000, v59
	v_med3_f32 v45, v45, s83, v238
	v_med3_f32 v44, v44, s83, v238
	global_store_dwordx2 v[80:81], v[76:77], off
	v_cvt_pk_fp8_f32 v43, v45, v44 op_sel:[0,0,1]
	ds_read2_b32 v[46:47], v50 offset0:16 offset1:24
	ds_read2_b32 v[48:49], v50 offset0:49 offset1:57
	ds_read2_b32 v[52:53], v50 offset0:82 offset1:90
	ds_read2_b32 v[54:55], v50 offset0:115 offset1:123
	v_lshl_add_u64 v[44:45], v[78:79], 0, v[18:19]
	global_store_dwordx2 v[44:45], v[42:43], off
	s_waitcnt lgkmcnt(3)
	v_mul_f32_e32 v42, 0x42000000, v46
	s_waitcnt lgkmcnt(2)
	v_mul_f32_e32 v43, 0x42000000, v48
	s_waitcnt lgkmcnt(1)
	v_mul_f32_e32 v44, 0x42000000, v52
	v_med3_f32 v45, v42, s83, v238
	v_med3_f32 v43, v43, s83, v238
	v_mov_b32_e32 v42, v0
	v_med3_f32 v48, v44, s83, v238
	v_cvt_pk_fp8_f32 v42, v45, v43
	ds_read2_b32 v[44:45], v50 offset0:148 offset1:156
	ds_read2_b32 v[56:57], v50 offset0:181 offset1:189
	ds_read2_b32 v[58:59], v50 offset0:214 offset1:222
	s_waitcnt lgkmcnt(3)
	v_mul_f32_e32 v46, 0x42000000, v54
	v_med3_f32 v43, v46, s83, v238
	ds_read2_b32 v[60:61], v50 offset0:247 offset1:255
	v_cvt_pk_fp8_f32 v42, v48, v43 op_sel:[0,0,1]
	s_waitcnt lgkmcnt(3)
	v_mul_f32_e32 v43, 0x42000000, v44
	s_waitcnt lgkmcnt(2)
	v_mul_f32_e32 v44, 0x42000000, v56
	v_med3_f32 v48, v43, s83, v238
	v_med3_f32 v44, v44, s83, v238
	v_mov_b32_e32 v43, v0
	v_cvt_pk_fp8_f32 v43, v48, v44
	s_waitcnt lgkmcnt(1)
	v_mul_f32_e32 v46, 0x42000000, v58
	s_waitcnt lgkmcnt(0)
	v_mul_f32_e32 v44, 0x42000000, v60
	v_med3_f32 v46, v46, s83, v238
	v_med3_f32 v44, v44, s83, v238
	v_cvt_pk_fp8_f32 v43, v46, v44 op_sel:[0,0,1]
	v_mul_f32_e32 v44, 0x42000000, v47
	v_mul_f32_e32 v46, 0x42000000, v49
	v_med3_f32 v48, v44, s83, v238
	v_med3_f32 v46, v46, s83, v238
	v_mov_b32_e32 v44, v0
	v_cvt_pk_fp8_f32 v44, v48, v46
	v_mul_f32_e32 v47, 0x42000000, v53
	v_mul_f32_e32 v46, 0x42000000, v55
	v_med3_f32 v47, v47, s83, v238
	v_med3_f32 v46, v46, s83, v238
	v_cvt_pk_fp8_f32 v44, v47, v46 op_sel:[0,0,1]
	v_mul_f32_e32 v45, 0x42000000, v45
	v_mul_f32_e32 v46, 0x42000000, v57
	v_med3_f32 v48, v45, s83, v238
	v_med3_f32 v46, v46, s83, v238
	v_mov_b32_e32 v45, v0
	v_cvt_pk_fp8_f32 v45, v48, v46
	v_mul_f32_e32 v47, 0x42000000, v59
	v_mul_f32_e32 v46, 0x42000000, v61
	v_med3_f32 v47, v47, s83, v238
	v_med3_f32 v46, v46, s83, v238
	v_cvt_pk_fp8_f32 v45, v47, v46 op_sel:[0,0,1]
	v_lshl_add_u64 v[46:47], v[78:79], 0, v[20:21]
	global_store_dwordx2 v[46:47], v[42:43], off
	v_lshl_add_u64 v[42:43], v[78:79], 0, v[22:23]
	global_store_dwordx2 v[42:43], v[44:45], off
	s_waitcnt lgkmcnt(0)
.LBB0_847:
	s_andn2_b64 vcc, exec, s[34:35]
	s_cbranch_vccnz .LBB0_849
	s_ashr_i32 s19, s60, 31
	s_mul_i32 s9, s60, 0x2a40000
	s_mul_hi_i32 s5, s60, 0x2a40000
	s_waitcnt lgkmcnt(0)
	s_add_u32 s26, s26, s9
	s_addc_u32 s27, s27, s5
	v_lshlrev_b32_e32 v42, 2, v4
	v_mov_b32_e32 v43, v0
	v_lshl_add_u64 v[42:43], s[26:27], 0, v[42:43]
	s_mov_b64 s[26:27], 0x1800
	v_lshl_add_u64 v[64:65], v[42:43], 0, s[26:27]
	v_lshl_add_u64 v[36:37], v[64:65], 0, v[36:37]
	v_lshl_add_u64 v[34:35], v[64:65], 0, v[34:35]
	global_load_dwordx4 v[42:45], v[36:37], off nt
	v_lshl_add_u64 v[32:33], v[64:65], 0, v[32:33]
	global_load_dwordx4 v[34:37], v[34:35], off nt
	s_mov_b32 s18, s60
	global_load_dwordx4 v[46:49], v[32:33], off nt
	v_mad_i64_i32 v[32:33], s[26:27], v41, s2, v[64:65]
	global_load_dwordx4 v[52:55], v[32:33], off nt
	v_mad_i64_i32 v[32:33], s[26:27], v40, s2, v[64:65]
	global_load_dwordx4 v[56:59], v[32:33], off nt
	v_mad_i64_i32 v[32:33], s[26:27], v39, s2, v[64:65]
	global_load_dwordx4 v[60:63], v[32:33], off nt
	v_mad_i64_i32 v[32:33], s[26:27], v38, s2, v[64:65]
	global_load_dwordx4 v[38:41], v[32:33], off nt
	v_mad_i64_i32 v[32:33], s[26:27], v3, s2, v[64:65]
	global_load_dwordx4 v[64:67], v[32:33], off nt
	v_add_u32_e32 v3, v1, v5
	v_add_u32_e32 v32, 0x420, v3
	s_lshl_b64 s[18:19], s[18:19], 17
	v_readlane_b32 s5, v255, 13
	s_add_u32 s5, s5, s18
	v_readlane_b32 s9, v255, 14
	s_addc_u32 s18, s9, s19
	s_mov_b32 s9, s61
	s_lshl_b64 s[8:9], s[8:9], 1
	s_add_u32 s8, s5, s8
	s_addc_u32 s9, s18, s9
	v_mov_b32_e32 v33, v0
	s_waitcnt vmcnt(7)
; #define LAS __attribute__((address_space(3)))
; __device__ __forceinline__ unsigned pk2(float lo, float hi) { return f2bf(lo) | (f2bf(hi) << 16); }
; __device__ __forceinline__ unsigned pk2q(float lo, float hi) { return f2bf(q8(lo)) | (f2bf(q8(hi)) << 16); }
; #define LDS_WAIT() asm volatile("s_waitcnt lgkmcnt(0)" ::: "memory")
; __device__ __forceinline__ void p0_transpose_item(const float* W, int ldw, int srccol0, int k0, bf16_t* dst, int K, LAS float* scr, int lane, bool q = false) {
;     ...
; #pragma unroll
;       for (int i = 0; i < 8; ++i) { LAS float* p = scr + (8 * i + (lane >> 3)) * 33 + 4 * (lane & 7); p[0] = v[i][0]; p[1] = v[i][1]; p[2] = v[i][2]; p[3] = v[i][3]; } }
;     LDS_WAIT(); asm volatile("" ::: "memory");
;     const int c = lane & 7;
; #pragma unroll
;     for (int j = 0; j < 4; ++j) { const int n = (lane >> 3) + 8 * j; const LAS float* s = scr + (8 * c) * 33 + n;
;         u32x4 o; if (q) { o.x = pk2q(s[0 * 33], s[1 * 33]); o.y = pk2q(s[2 * 33], s[3 * 33]); o.z = pk2q(s[4 * 33], s[5 * 33]); o.w = pk2q(s[6 * 33], s[7 * 33]); }
;         else { o.x = pk2(s[0 * 33], s[1 * 33]); o.y = pk2(s[2 * 33], s[3 * 33]); o.z = pk2(s[4 * 33], s[5 * 33]); o.w = pk2(s[6 * 33], s[7 * 33]); }
;         *(u32x4*)(dst + (size_t)n * K + k0 + 8 * c) = o; }
;     LDS_WAIT(); asm volatile("" ::: "memory");
; }
	ds_write2_b32 v3, v42, v43 offset1:1
	ds_write2_b32 v3, v44, v45 offset0:2 offset1:3
	s_waitcnt vmcnt(6)
	ds_write2_b32 v32, v34, v35 offset1:1
	v_add_u32_e32 v32, 0x428, v3
	ds_write2_b32 v32, v36, v37 offset1:1
	v_add_u32_e32 v32, 0x840, v3
	s_waitcnt vmcnt(5)
	ds_write2_b32 v32, v46, v47 offset1:1
	v_add_u32_e32 v32, 0x848, v3
	ds_write2_b32 v32, v48, v49 offset1:1
	v_add_u32_e32 v32, 0xc60, v3
	s_waitcnt vmcnt(4)
	ds_write2_b32 v32, v52, v53 offset1:1
	v_add_u32_e32 v32, 0xc68, v3
	ds_write2_b32 v32, v54, v55 offset1:1
	v_add_u32_e32 v32, 0x1080, v3
	s_waitcnt vmcnt(3)
	ds_write2_b32 v32, v56, v57 offset1:1
	v_add_u32_e32 v32, 0x1088, v3
	ds_write2_b32 v32, v58, v59 offset1:1
	v_add_u32_e32 v32, 0x14a0, v3
	s_waitcnt vmcnt(2)
	ds_write2_b32 v32, v60, v61 offset1:1
	v_add_u32_e32 v32, 0x14a8, v3
	ds_write2_b32 v32, v62, v63 offset1:1
	v_add_u32_e32 v32, 0x18c0, v3
	s_waitcnt vmcnt(1)
	ds_write2_b32 v32, v38, v39 offset1:1
	v_add_u32_e32 v32, 0x18c8, v3
	ds_write2_b32 v32, v40, v41 offset1:1
	v_add_u32_e32 v32, 0x1ce0, v3
	v_add_u32_e32 v3, 0x1ce8, v3
	s_waitcnt vmcnt(0)
	ds_write2_b32 v32, v64, v65 offset1:1
	ds_write2_b32 v3, v66, v67 offset1:1
	s_waitcnt lgkmcnt(0)
	ds_read2_b32 v[38:39], v50 offset0:33 offset1:41
	ds_read2_b32 v[40:41], v50 offset1:8
	ds_read2_b32 v[42:43], v50 offset0:66 offset1:74
	ds_read2_b32 v[44:45], v50 offset0:99 offset1:107
	ds_read2_b32 v[46:47], v50 offset0:132 offset1:140
	ds_read2_b32 v[48:49], v50 offset0:165 offset1:173
	ds_read2_b32 v[52:53], v50 offset0:198 offset1:206
	ds_read2_b32 v[54:55], v50 offset0:231 offset1:239
	s_waitcnt lgkmcnt(7)
	v_bfe_u32 v34, v38, 16, 1
	s_waitcnt lgkmcnt(6)
	v_bfe_u32 v3, v40, 16, 1
	v_add3_u32 v3, v40, v3, s23
	v_lshrrev_b32_e32 v3, 16, v3
	v_add3_u32 v34, v38, v34, s23
	v_and_or_b32 v34, v34, s95, v3
	s_waitcnt lgkmcnt(5)
	v_bfe_u32 v3, v42, 16, 1
	v_add3_u32 v3, v42, v3, s23
	s_waitcnt lgkmcnt(4)
	v_bfe_u32 v35, v44, 16, 1
	v_lshrrev_b32_e32 v3, 16, v3
	v_add3_u32 v35, v44, v35, s23
	v_and_or_b32 v35, v35, s95, v3
	s_waitcnt lgkmcnt(3)
	v_bfe_u32 v3, v46, 16, 1
	v_add3_u32 v3, v46, v3, s23
	s_waitcnt lgkmcnt(2)
	v_bfe_u32 v36, v48, 16, 1
	v_lshrrev_b32_e32 v3, 16, v3
	v_add3_u32 v36, v48, v36, s23
	v_and_or_b32 v36, v36, s95, v3
	s_waitcnt lgkmcnt(1)
	v_bfe_u32 v3, v52, 16, 1
	v_lshlrev_b32_e32 v32, 1, v6
	v_add3_u32 v3, v52, v3, s23
	s_waitcnt lgkmcnt(0)
	v_bfe_u32 v37, v54, 16, 1
	v_lshl_add_u64 v[32:33], s[8:9], 0, v[32:33]
	v_lshrrev_b32_e32 v3, 16, v3
	v_add3_u32 v37, v54, v37, s23
	v_and_or_b32 v37, v37, s95, v3
	v_lshl_add_u64 v[56:57], v[32:33], 0, v[24:25]
	v_bfe_u32 v3, v41, 16, 1
	global_store_dwordx4 v[56:57], v[34:37], off
	v_add3_u32 v3, v41, v3, s23
	v_lshrrev_b32_e32 v3, 16, v3
	v_bfe_u32 v34, v39, 16, 1
	v_add3_u32 v34, v39, v34, s23
	v_and_or_b32 v34, v34, s95, v3
	v_bfe_u32 v3, v43, 16, 1
	v_add3_u32 v3, v43, v3, s23
	v_bfe_u32 v35, v45, 16, 1
	v_lshrrev_b32_e32 v3, 16, v3
	v_add3_u32 v35, v45, v35, s23
	v_and_or_b32 v35, v35, s95, v3
	v_bfe_u32 v3, v47, 16, 1
	v_add3_u32 v3, v47, v3, s23
	v_bfe_u32 v36, v49, 16, 1
	v_lshrrev_b32_e32 v3, 16, v3
	v_add3_u32 v36, v49, v36, s23
	v_and_or_b32 v36, v36, s95, v3
	v_bfe_u32 v3, v53, 16, 1
	v_add3_u32 v3, v53, v3, s23
	v_bfe_u32 v37, v55, 16, 1
	v_lshrrev_b32_e32 v3, 16, v3
	v_add3_u32 v37, v55, v37, s23
	v_and_or_b32 v37, v37, s95, v3
	v_lshl_add_u64 v[38:39], v[32:33], 0, v[26:27]
	global_store_dwordx4 v[38:39], v[34:37], off
	ds_read2_b32 v[38:39], v50 offset0:49 offset1:57
	ds_read2_b32 v[40:41], v50 offset0:16 offset1:24
	ds_read2_b32 v[42:43], v50 offset0:82 offset1:90
	ds_read2_b32 v[44:45], v50 offset0:115 offset1:123
	ds_read2_b32 v[46:47], v50 offset0:148 offset1:156
	ds_read2_b32 v[48:49], v50 offset0:181 offset1:189
	ds_read2_b32 v[52:53], v50 offset0:214 offset1:222
	ds_read2_b32 v[54:55], v50 offset0:247 offset1:255
	s_waitcnt lgkmcnt(7)
	v_bfe_u32 v34, v38, 16, 1
	s_waitcnt lgkmcnt(6)
	v_bfe_u32 v3, v40, 16, 1
	v_add3_u32 v3, v40, v3, s23
	v_lshrrev_b32_e32 v3, 16, v3
	v_add3_u32 v34, v38, v34, s23
	v_and_or_b32 v34, v34, s95, v3
	s_waitcnt lgkmcnt(5)
	v_bfe_u32 v3, v42, 16, 1
	v_add3_u32 v3, v42, v3, s23
	s_waitcnt lgkmcnt(4)
	v_bfe_u32 v35, v44, 16, 1
	v_lshrrev_b32_e32 v3, 16, v3
	v_add3_u32 v35, v44, v35, s23
	v_and_or_b32 v35, v35, s95, v3
	s_waitcnt lgkmcnt(3)
	v_bfe_u32 v3, v46, 16, 1
	v_add3_u32 v3, v46, v3, s23
	s_waitcnt lgkmcnt(2)
	v_bfe_u32 v36, v48, 16, 1
	v_lshrrev_b32_e32 v3, 16, v3
	v_add3_u32 v36, v48, v36, s23
	v_and_or_b32 v36, v36, s95, v3
	s_waitcnt lgkmcnt(1)
	v_bfe_u32 v3, v52, 16, 1
	v_add3_u32 v3, v52, v3, s23
	s_waitcnt lgkmcnt(0)
	v_bfe_u32 v37, v54, 16, 1
	v_lshrrev_b32_e32 v3, 16, v3
	v_add3_u32 v37, v54, v37, s23
	v_and_or_b32 v37, v37, s95, v3
	v_lshl_add_u64 v[56:57], v[32:33], 0, v[28:29]
	v_bfe_u32 v3, v41, 16, 1
	global_store_dwordx4 v[56:57], v[34:37], off
	v_add3_u32 v3, v41, v3, s23
	v_lshrrev_b32_e32 v3, 16, v3
	v_bfe_u32 v34, v39, 16, 1
	v_add3_u32 v34, v39, v34, s23
	v_and_or_b32 v34, v34, s95, v3
	v_bfe_u32 v3, v43, 16, 1
	v_add3_u32 v3, v43, v3, s23
	v_bfe_u32 v35, v45, 16, 1
	v_lshrrev_b32_e32 v3, 16, v3
	v_add3_u32 v35, v45, v35, s23
	v_and_or_b32 v35, v35, s95, v3
	v_bfe_u32 v3, v47, 16, 1
	v_add3_u32 v3, v47, v3, s23
	v_bfe_u32 v36, v49, 16, 1
	v_lshrrev_b32_e32 v3, 16, v3
	v_add3_u32 v36, v49, v36, s23
	v_and_or_b32 v36, v36, s95, v3
	v_bfe_u32 v3, v53, 16, 1
	v_add3_u32 v3, v53, v3, s23
	v_bfe_u32 v37, v55, 16, 1
	v_lshrrev_b32_e32 v3, 16, v3
	v_add3_u32 v37, v55, v37, s23
	v_and_or_b32 v37, v37, s95, v3
	v_lshl_add_u64 v[32:33], v[32:33], 0, v[30:31]
	global_store_dwordx4 v[32:33], v[34:37], off
	s_waitcnt lgkmcnt(0)

; #define LAS __attribute__((address_space(3)))
; #define LDS_WAIT() asm volatile("s_waitcnt lgkmcnt(0)" ::: "memory")
; __device__ __forceinline__ void p0_transpose_item8(const float* W, int ldw, int srccol0, int k0, unsigned char* dst, int K, LAS float* scr, int lane) {
;     { f32x4 v[8];
; #pragma unroll
;       for (int i = 0; i < 8; ++i) v[i] = *(const f32x4*)(W + (size_t)(k0 + 8 * i + (lane >> 3)) * ldw + srccol0 + 4 * (lane & 7));
; #pragma unroll
;       for (int i = 0; i < 8; ++i) { LAS float* p = scr + (8 * i + (lane >> 3)) * 33 + 4 * (lane & 7); p[0] = v[i][0]; p[1] = v[i][1]; p[2] = v[i][2]; p[3] = v[i][3]; } }
;     LDS_WAIT(); asm volatile("" ::: "memory");
;     const int c = lane & 7;
; #pragma unroll
;     for (int j = 0; j < 4; ++j) { const int n = (lane >> 3) + 8 * j; const LAS float* s = scr + (8 * c) * 33 + n;
;         u32x2 o; o.x = pk4_f8(s[0 * 33] * 32.f, s[1 * 33] * 32.f, s[2 * 33] * 32.f, s[3 * 33] * 32.f); o.y = pk4_f8(s[4 * 33] * 32.f, s[5 * 33] * 32.f, s[6 * 33] * 32.f, s[7 * 33] * 32.f);
;         *(u32x2*)(dst + (size_t)n * K + k0 + 8 * c) = o; }
;     LDS_WAIT(); asm volatile("" ::: "memory");
; __device__ __forceinline__ void p0_item(KP Pk, Frame& F, int it, LAS float* scr) {
;     ...
;         if (r < TI_WIN) { const int kb = r / 168, nb = r % 168, n0 = 32 * nb;
;             if (WIN_F8_L(l)) p0_transpose_item8(Pk->in[I_WIN] + (size_t)l * D * DIN, DIN, n0 < 1536 ? n0 : n0 + 32, 64 * kb, ws + WS_WIN + (size_t)l * NU * D * 2 + (size_t)n0 * D, D, scr, F.lane);
.LBB0_850:
	s_andn2_b64 vcc, exec, s[8:9]
	s_cbranch_vccnz .LBB0_819
	s_mul_i32 s5, s4, 0xffffc30d
	s_lshr_b32 s5, s5, 16
	s_add_i32 s5, s5, s4
	s_sext_i32_i16 s8, s5
	s_ashr_i32 s8, s8, 7
	s_bfe_u32 s5, s5, 0x1000f
	s_add_i32 s5, s8, s5
	s_sext_i32_i16 s8, s5
	s_mulk_i32 s5, 0xa8
	s_sub_i32 s4, s4, s5
	s_sext_i32_i16 s4, s4
	s_lshl_b32 s34, s4, 5
	s_add_i32 s5, s34, 32
	s_cmp_lt_i32 s4, 48
	s_waitcnt lgkmcnt(0)
	s_cselect_b32 s26, s34, s5
	s_lshl_b32 s8, s8, 6
	s_load_dwordx2 s[38:39], s[48:49], 0x40
	v_add_u32_e32 v3, s8, v2
	v_add_u32_e32 v32, 8, v3
	s_ashr_i32 s27, s26, 31
	v_mad_i64_i32 v[34:35], s[4:5], v3, s2, 0
	v_mad_i64_i32 v[32:33], s[4:5], v32, s2, 0
	v_add_u32_e32 v62, 16, v3
	v_add_u32_e32 v61, 24, v3
	v_add_u32_e32 v60, 32, v3
	v_add_u32_e32 v59, 40, v3
	v_add_u32_e32 v58, 48, v3
	v_add_u32_e32 v57, 56, v3
	v_add_u32_e32 v3, v1, v5
	s_cmp_gt_u32 s60, 1
	s_mov_b64 s[40:41], -1
	s_mul_i32 s4, s60, 0x2a40000
	v_lshlrev_b32_e32 v36, 2, v4
	v_add_u32_e32 v42, 0x420, v3
	v_add_u32_e32 v43, 0x428, v3
	v_add_u32_e32 v44, 0x840, v3
	v_add_u32_e32 v45, 0x848, v3
	v_add_u32_e32 v46, 0xc60, v3
	v_add_u32_e32 v47, 0xc68, v3
	v_add_u32_e32 v48, 0x1080, v3
	v_add_u32_e32 v49, 0x1088, v3
	v_add_u32_e32 v51, 0x14a0, v3
	v_add_u32_e32 v52, 0x14a8, v3
	v_add_u32_e32 v53, 0x18c0, v3
	v_add_u32_e32 v54, 0x18c8, v3
	v_add_u32_e32 v55, 0x1ce0, v3
	v_add_u32_e32 v56, 0x1ce8, v3
	s_cbranch_scc1 .LBB0_853
	s_mul_hi_u32 s5, s60, 0x2a40000
	s_waitcnt lgkmcnt(0)
	s_add_u32 s9, s38, s4
	s_addc_u32 s5, s39, s5
	s_mul_i32 s19, s60, 0x1500000
	v_readlane_b32 s35, v255, 15
	s_mul_hi_u32 s18, s60, 0x1500000
	s_add_u32 s37, s35, s19
	v_readlane_b32 s19, v255, 16
	s_addc_u32 s40, s19, s18
	s_ashr_i32 s35, s34, 31
	s_lshl_b64 s[18:19], s[34:35], 11
	s_add_u32 s35, s37, s18
	s_addc_u32 s37, s40, s19
	s_lshl_b64 s[18:19], s[26:27], 2
	s_add_u32 s18, s9, s18
	s_addc_u32 s19, s5, s19
	v_mov_b32_e32 v37, v0
	v_lshl_add_u64 v[88:89], s[18:19], 0, v[36:37]
	v_lshl_add_u64 v[38:39], v[88:89], 0, v[34:35]
	global_load_dwordx4 v[38:41], v[38:39], off nt
	v_lshl_add_u64 v[64:65], v[88:89], 0, v[32:33]
	global_load_dwordx4 v[64:67], v[64:65], off nt
	v_mad_i64_i32 v[68:69], s[18:19], v62, s2, v[88:89]
	global_load_dwordx4 v[68:71], v[68:69], off nt
	v_mad_i64_i32 v[72:73], s[18:19], v61, s2, v[88:89]
	global_load_dwordx4 v[72:75], v[72:73], off nt
	v_mad_i64_i32 v[76:77], s[18:19], v60, s2, v[88:89]
	global_load_dwordx4 v[76:79], v[76:77], off nt
	v_mad_i64_i32 v[80:81], s[18:19], v59, s2, v[88:89]
	global_load_dwordx4 v[80:83], v[80:81], off nt
	v_mad_i64_i32 v[84:85], s[18:19], v58, s2, v[88:89]
	global_load_dwordx4 v[84:87], v[84:85], off nt
	v_mad_i64_i32 v[88:89], s[18:19], v57, s2, v[88:89]
	global_load_dwordx4 v[88:91], v[88:89], off nt
	s_ashr_i32 s5, s8, 31
	s_add_u32 s18, s35, s8
	s_addc_u32 s19, s37, s5
	s_mov_b64 s[40:41], 0
	s_waitcnt vmcnt(7)
	ds_write2_b32 v3, v38, v39 offset1:1
	ds_write2_b32 v3, v40, v41 offset0:2 offset1:3
	s_waitcnt vmcnt(6)
	ds_write2_b32 v42, v64, v65 offset1:1
	ds_write2_b32 v43, v66, v67 offset1:1
	s_waitcnt vmcnt(5)
	ds_write2_b32 v44, v68, v69 offset1:1
	ds_write2_b32 v45, v70, v71 offset1:1
	s_waitcnt vmcnt(4)
	ds_write2_b32 v46, v72, v73 offset1:1
	ds_write2_b32 v47, v74, v75 offset1:1
	s_waitcnt vmcnt(3)
	ds_write2_b32 v48, v76, v77 offset1:1
	ds_write2_b32 v49, v78, v79 offset1:1
	s_waitcnt vmcnt(2)
	ds_write2_b32 v51, v80, v81 offset1:1
	ds_write2_b32 v52, v82, v83 offset1:1
	s_waitcnt vmcnt(1)
	ds_write2_b32 v53, v84, v85 offset1:1
	ds_write2_b32 v54, v86, v87 offset1:1
	s_waitcnt vmcnt(0)
	ds_write2_b32 v55, v88, v89 offset1:1
	ds_write2_b32 v56, v90, v91 offset1:1
	s_waitcnt lgkmcnt(0)
	ds_read2_b32 v[40:41], v50 offset1:8
	ds_read2_b32 v[64:65], v50 offset0:33 offset1:41
	ds_read2_b32 v[72:73], v50 offset0:132 offset1:140
	ds_read2_b32 v[74:75], v50 offset0:165 offset1:173
	ds_read2_b32 v[66:67], v50 offset0:66 offset1:74
	ds_read2_b32 v[68:69], v50 offset0:99 offset1:107
	s_waitcnt lgkmcnt(5)
	v_mul_f32_e32 v37, 0x42000000, v40
	s_waitcnt lgkmcnt(4)
	v_mul_f32_e32 v40, 0x42000000, v64
	v_med3_f32 v37, v37, s83, v238
	v_med3_f32 v40, v40, s83, v238
	v_mov_b32_e32 v70, v0
	ds_read2_b32 v[76:77], v50 offset0:198 offset1:206
	ds_read2_b32 v[78:79], v50 offset0:231 offset1:239
	v_cvt_pk_fp8_f32 v70, v37, v40
	s_waitcnt lgkmcnt(5)
	v_mul_f32_e32 v37, 0x42000000, v72
	s_waitcnt lgkmcnt(4)
	v_mul_f32_e32 v40, 0x42000000, v74
	v_med3_f32 v37, v37, s83, v238
	v_med3_f32 v40, v40, s83, v238
	v_mov_b32_e32 v71, v0
	s_waitcnt lgkmcnt(3)
	v_mul_f32_e32 v63, 0x42000000, v66
	s_waitcnt lgkmcnt(2)
	v_mul_f32_e32 v64, 0x42000000, v68
	v_cvt_pk_fp8_f32 v71, v37, v40
	v_med3_f32 v63, v63, s83, v238
	v_med3_f32 v64, v64, s83, v238
	v_cvt_pk_fp8_f32 v70, v63, v64 op_sel:[0,0,1]
	s_waitcnt lgkmcnt(1)
	v_mul_f32_e32 v63, 0x42000000, v76
	s_waitcnt lgkmcnt(0)
	v_mul_f32_e32 v64, 0x42000000, v78
	v_med3_f32 v63, v63, s83, v238
	v_med3_f32 v64, v64, s83, v238
	v_mul_f32_e32 v37, 0x42000000, v41
	v_mul_f32_e32 v40, 0x42000000, v65
	v_cvt_pk_fp8_f32 v71, v63, v64 op_sel:[0,0,1]
	v_med3_f32 v37, v37, s83, v238
	v_med3_f32 v64, v40, s83, v238
	v_mov_b32_e32 v40, v0
	v_cvt_pk_fp8_f32 v40, v37, v64
	v_mul_f32_e32 v41, 0x42000000, v67
	v_mul_f32_e32 v63, 0x42000000, v69
	v_med3_f32 v41, v41, s83, v238
	v_med3_f32 v63, v63, s83, v238
	v_cvt_pk_fp8_f32 v40, v41, v63 op_sel:[0,0,1]
	v_mul_f32_e32 v37, 0x42000000, v73
	v_mul_f32_e32 v41, 0x42000000, v75
	v_med3_f32 v37, v37, s83, v238
	v_med3_f32 v65, v41, s83, v238
	v_mov_b32_e32 v41, v0
	v_cvt_pk_fp8_f32 v41, v37, v65
	v_mul_f32_e32 v63, 0x42000000, v77
	v_mul_f32_e32 v64, 0x42000000, v79
	v_med3_f32 v63, v63, s83, v238
	v_med3_f32 v64, v64, s83, v238
	v_cvt_pk_fp8_f32 v41, v63, v64 op_sel:[0,0,1]
	v_lshl_add_u64 v[38:39], s[18:19], 0, v[6:7]
	v_lshl_add_u64 v[64:65], v[38:39], 0, v[18:19]
	ds_read2_b32 v[72:73], v50 offset0:148 offset1:156
	global_store_dwordx2 v[64:65], v[40:41], off
	ds_read2_b32 v[40:41], v50 offset0:16 offset1:24
	ds_read2_b32 v[64:65], v50 offset0:49 offset1:57
	ds_read2_b32 v[74:75], v50 offset0:181 offset1:189
	ds_read2_b32 v[66:67], v50 offset0:82 offset1:90
	ds_read2_b32 v[68:69], v50 offset0:115 offset1:123
	v_lshl_add_u64 v[80:81], v[38:39], 0, v[16:17]
	s_waitcnt lgkmcnt(4)
; #define LAS __attribute__((address_space(3)))
; #define LDS_WAIT() asm volatile("s_waitcnt lgkmcnt(0)" ::: "memory")
; __device__ __forceinline__ void p0_transpose_item8(const float* W, int ldw, int srccol0, int k0, unsigned char* dst, int K, LAS float* scr, int lane) {
;     ...
;     const int c = lane & 7;
; #pragma unroll
;     for (int j = 0; j < 4; ++j) { const int n = (lane >> 3) + 8 * j; const LAS float* s = scr + (8 * c) * 33 + n;
;         u32x2 o; o.x = pk4_f8(s[0 * 33] * 32.f, s[1 * 33] * 32.f, s[2 * 33] * 32.f, s[3 * 33] * 32.f); o.y = pk4_f8(s[4 * 33] * 32.f, s[5 * 33] * 32.f, s[6 * 33] * 32.f, s[7 * 33] * 32.f);
;         *(u32x2*)(dst + (size_t)n * K + k0 + 8 * c) = o; }
;     LDS_WAIT(); asm volatile("" ::: "memory");
	v_mul_f32_e32 v37, 0x42000000, v40
	s_waitcnt lgkmcnt(3)
	v_mul_f32_e32 v40, 0x42000000, v64
	global_store_dwordx2 v[80:81], v[70:71], off
	v_med3_f32 v37, v37, s83, v238
	v_med3_f32 v40, v40, s83, v238
	v_mov_b32_e32 v70, v0
	ds_read2_b32 v[76:77], v50 offset0:214 offset1:222
	ds_read2_b32 v[78:79], v50 offset0:247 offset1:255
	v_cvt_pk_fp8_f32 v70, v37, v40
	v_mul_f32_e32 v37, 0x42000000, v72
	s_waitcnt lgkmcnt(4)
	v_mul_f32_e32 v40, 0x42000000, v74
	v_med3_f32 v37, v37, s83, v238
	v_med3_f32 v40, v40, s83, v238
	v_mov_b32_e32 v71, v0
	s_waitcnt lgkmcnt(3)
	v_mul_f32_e32 v63, 0x42000000, v66
	s_waitcnt lgkmcnt(2)
	v_mul_f32_e32 v64, 0x42000000, v68
	v_cvt_pk_fp8_f32 v71, v37, v40
	v_med3_f32 v63, v63, s83, v238
	v_med3_f32 v64, v64, s83, v238
	v_cvt_pk_fp8_f32 v70, v63, v64 op_sel:[0,0,1]
	s_waitcnt lgkmcnt(1)
	v_mul_f32_e32 v63, 0x42000000, v76
	s_waitcnt lgkmcnt(0)
	v_mul_f32_e32 v64, 0x42000000, v78
	v_med3_f32 v63, v63, s83, v238
	v_med3_f32 v64, v64, s83, v238
	v_mul_f32_e32 v37, 0x42000000, v41
	v_mul_f32_e32 v40, 0x42000000, v65
	v_cvt_pk_fp8_f32 v71, v63, v64 op_sel:[0,0,1]
	v_med3_f32 v37, v37, s83, v238
	v_med3_f32 v64, v40, s83, v238
	v_mov_b32_e32 v40, v0
	v_cvt_pk_fp8_f32 v40, v37, v64
	v_mul_f32_e32 v41, 0x42000000, v67
	v_mul_f32_e32 v63, 0x42000000, v69
	v_med3_f32 v41, v41, s83, v238
	v_med3_f32 v63, v63, s83, v238
	v_cvt_pk_fp8_f32 v40, v41, v63 op_sel:[0,0,1]
	v_mul_f32_e32 v37, 0x42000000, v73
	v_mul_f32_e32 v41, 0x42000000, v75
	v_med3_f32 v37, v37, s83, v238
	v_med3_f32 v65, v41, s83, v238
	v_mov_b32_e32 v41, v0
	v_cvt_pk_fp8_f32 v41, v37, v65
	v_mul_f32_e32 v63, 0x42000000, v77
	v_mul_f32_e32 v64, 0x42000000, v79
	v_med3_f32 v63, v63, s83, v238
	v_med3_f32 v64, v64, s83, v238
	v_cvt_pk_fp8_f32 v41, v63, v64 op_sel:[0,0,1]
	v_lshl_add_u64 v[80:81], v[38:39], 0, v[20:21]
	v_lshl_add_u64 v[38:39], v[38:39], 0, v[22:23]
	global_store_dwordx2 v[80:81], v[70:71], off
	global_store_dwordx2 v[38:39], v[40:41], off
	s_waitcnt lgkmcnt(0)
; #define LAS __attribute__((address_space(3)))
; __device__ __forceinline__ unsigned pk2(float lo, float hi) { return f2bf(lo) | (f2bf(hi) << 16); }
; __device__ __forceinline__ unsigned pk2q(float lo, float hi) { return f2bf(q8(lo)) | (f2bf(q8(hi)) << 16); }
; #define LDS_WAIT() asm volatile("s_waitcnt lgkmcnt(0)" ::: "memory")
; __device__ __forceinline__ void p0_transpose_item(const float* W, int ldw, int srccol0, int k0, bf16_t* dst, int K, LAS float* scr, int lane, bool q = false) {
;     { f32x4 v[8];
; #pragma unroll
;       for (int i = 0; i < 8; ++i) v[i] = *(const f32x4*)(W + (size_t)(k0 + 8 * i + (lane >> 3)) * ldw + srccol0 + 4 * (lane & 7));
; #pragma unroll
;       for (int i = 0; i < 8; ++i) { LAS float* p = scr + (8 * i + (lane >> 3)) * 33 + 4 * (lane & 7); p[0] = v[i][0]; p[1] = v[i][1]; p[2] = v[i][2]; p[3] = v[i][3]; } }
;     LDS_WAIT(); asm volatile("" ::: "memory");
;     const int c = lane & 7;
; #pragma unroll
;     for (int j = 0; j < 4; ++j) { const int n = (lane >> 3) + 8 * j; const LAS float* s = scr + (8 * c) * 33 + n;
;         u32x4 o; if (q) { o.x = pk2q(s[0 * 33], s[1 * 33]); o.y = pk2q(s[2 * 33], s[3 * 33]); o.z = pk2q(s[4 * 33], s[5 * 33]); o.w = pk2q(s[6 * 33], s[7 * 33]); }
;         else { o.x = pk2(s[0 * 33], s[1 * 33]); o.y = pk2(s[2 * 33], s[3 * 33]); o.z = pk2(s[4 * 33], s[5 * 33]); o.w = pk2(s[6 * 33], s[7 * 33]); }
;         *(u32x4*)(dst + (size_t)n * K + k0 + 8 * c) = o; }
;     LDS_WAIT(); asm volatile("" ::: "memory");
; }
; __device__ __forceinline__ void p0_item(KP Pk, Frame& F, int it, LAS float* scr) {
;     ...
;             else p0_transpose_item(Pk->in[I_WIN] + (size_t)l * D * DIN, DIN, n0 < 1536 ? n0 : n0 + 32, 64 * kb, (bf16_t*)(ws + WS_WIN) + ((size_t)l * NU + n0) * D, D, scr, F.lane); return; }
.LBB0_853:
	s_andn2_b64 vcc, exec, s[40:41]
	s_cbranch_vccnz .LBB0_819
	s_mul_hi_i32 s5, s60, 0x2a40000
	s_waitcnt lgkmcnt(0)
	s_add_u32 s9, s38, s4
	s_addc_u32 s18, s39, s5
	s_mul_i32 s4, s60, 0x1500
	s_ashr_i32 s19, s34, 31
	s_mul_hi_i32 s5, s60, 0x1500
	s_add_u32 s4, s4, s34
	s_addc_u32 s5, s5, s19
	s_lshl_b64 s[4:5], s[4:5], 12
	v_readlane_b32 s19, v255, 15
	s_add_u32 s19, s19, s4
	v_readlane_b32 s4, v255, 16
	s_addc_u32 s34, s4, s5
	s_lshl_b64 s[4:5], s[26:27], 2
	s_add_u32 s4, s9, s4
	s_addc_u32 s5, s18, s5
	v_mov_b32_e32 v37, v0
	v_lshl_add_u64 v[78:79], s[4:5], 0, v[36:37]
	v_lshl_add_u64 v[34:35], v[78:79], 0, v[34:35]
	global_load_dwordx4 v[34:37], v[34:35], off nt
	v_lshl_add_u64 v[32:33], v[78:79], 0, v[32:33]
	global_load_dwordx4 v[38:41], v[32:33], off nt
	v_mad_i64_i32 v[32:33], s[4:5], v62, s2, v[78:79]
	global_load_dwordx4 v[62:65], v[32:33], off nt
	v_mad_i64_i32 v[32:33], s[4:5], v61, s2, v[78:79]
	global_load_dwordx4 v[66:69], v[32:33], off nt
	v_mad_i64_i32 v[32:33], s[4:5], v60, s2, v[78:79]
	global_load_dwordx4 v[70:73], v[32:33], off nt
	v_mad_i64_i32 v[32:33], s[4:5], v59, s2, v[78:79]
	global_load_dwordx4 v[74:77], v[32:33], off nt
	v_mad_i64_i32 v[32:33], s[4:5], v58, s2, v[78:79]
	global_load_dwordx4 v[58:61], v[32:33], off nt
	v_mad_i64_i32 v[32:33], s[4:5], v57, s2, v[78:79]
	global_load_dwordx4 v[78:81], v[32:33], off nt
	s_ashr_i32 s9, s8, 31
	s_lshl_b64 s[4:5], s[8:9], 1
	s_add_u32 s8, s19, s4
	s_addc_u32 s9, s34, s5
	v_lshlrev_b32_e32 v32, 1, v6
	v_mov_b32_e32 v33, v0
	v_lshl_add_u64 v[32:33], s[8:9], 0, v[32:33]
	s_waitcnt vmcnt(7)
	ds_write2_b32 v3, v34, v35 offset1:1
	ds_write2_b32 v3, v36, v37 offset0:2 offset1:3
	s_waitcnt vmcnt(6)
	ds_write2_b32 v42, v38, v39 offset1:1
	ds_write2_b32 v43, v40, v41 offset1:1
	s_waitcnt vmcnt(5)
	ds_write2_b32 v44, v62, v63 offset1:1
	ds_write2_b32 v45, v64, v65 offset1:1
	s_waitcnt vmcnt(4)
	ds_write2_b32 v46, v66, v67 offset1:1
	ds_write2_b32 v47, v68, v69 offset1:1
	s_waitcnt vmcnt(3)
	ds_write2_b32 v48, v70, v71 offset1:1
	ds_write2_b32 v49, v72, v73 offset1:1
	s_waitcnt vmcnt(2)
	ds_write2_b32 v51, v74, v75 offset1:1
	ds_write2_b32 v52, v76, v77 offset1:1
	s_waitcnt vmcnt(1)
	ds_write2_b32 v53, v58, v59 offset1:1
	ds_write2_b32 v54, v60, v61 offset1:1
	s_waitcnt vmcnt(0)
	ds_write2_b32 v55, v78, v79 offset1:1
	ds_write2_b32 v56, v80, v81 offset1:1
	s_waitcnt lgkmcnt(0)
	ds_read2_b32 v[46:47], v50 offset0:33 offset1:41
	ds_read2_b32 v[48:49], v50 offset1:8
	v_lshl_add_u64 v[56:57], v[32:33], 0, v[24:25]
	s_waitcnt lgkmcnt(1)
	v_bfe_u32 v34, v46, 16, 1
	s_waitcnt lgkmcnt(0)
	v_bfe_u32 v3, v48, 16, 1
	v_add3_u32 v3, v48, v3, s23
	v_lshrrev_b32_e32 v3, 16, v3
	v_add3_u32 v34, v46, v34, s23
	v_and_or_b32 v52, v34, s95, v3
	ds_read2_b32 v[36:37], v50 offset0:66 offset1:74
	ds_read2_b32 v[34:35], v50 offset0:99 offset1:107
	ds_read2_b32 v[40:41], v50 offset0:132 offset1:140
	ds_read2_b32 v[38:39], v50 offset0:165 offset1:173
	ds_read2_b32 v[44:45], v50 offset0:198 offset1:206
	ds_read2_b32 v[42:43], v50 offset0:231 offset1:239
	s_waitcnt lgkmcnt(5)
	v_bfe_u32 v3, v36, 16, 1
	v_add3_u32 v3, v36, v3, s23
	s_waitcnt lgkmcnt(4)
	v_bfe_u32 v36, v34, 16, 1
	v_lshrrev_b32_e32 v3, 16, v3
	v_add3_u32 v34, v34, v36, s23
	v_and_or_b32 v53, v34, s95, v3
	s_waitcnt lgkmcnt(3)
	v_bfe_u32 v3, v40, 16, 1
	v_add3_u32 v3, v40, v3, s23
	s_waitcnt lgkmcnt(2)
	v_bfe_u32 v34, v38, 16, 1
	v_lshrrev_b32_e32 v3, 16, v3
	v_add3_u32 v34, v38, v34, s23
	v_and_or_b32 v54, v34, s95, v3
	s_waitcnt lgkmcnt(1)
	v_bfe_u32 v3, v44, 16, 1
	v_add3_u32 v3, v44, v3, s23
	s_waitcnt lgkmcnt(0)
	v_bfe_u32 v34, v42, 16, 1
	v_lshrrev_b32_e32 v3, 16, v3
	v_add3_u32 v34, v42, v34, s23
	v_and_or_b32 v55, v34, s95, v3
	v_bfe_u32 v3, v49, 16, 1
	v_add3_u32 v3, v49, v3, s23
	v_bfe_u32 v34, v47, 16, 1
	v_lshrrev_b32_e32 v3, 16, v3
	v_add3_u32 v34, v47, v34, s23
	v_and_or_b32 v34, v34, s95, v3
	v_bfe_u32 v3, v37, 16, 1
	v_add3_u32 v3, v37, v3, s23
	v_bfe_u32 v36, v35, 16, 1
	v_lshrrev_b32_e32 v3, 16, v3
	v_add3_u32 v35, v35, v36, s23
	v_and_or_b32 v35, v35, s95, v3
	v_bfe_u32 v3, v41, 16, 1
	v_add3_u32 v3, v41, v3, s23
	v_bfe_u32 v36, v39, 16, 1
	v_lshrrev_b32_e32 v3, 16, v3
	v_add3_u32 v36, v39, v36, s23
	v_and_or_b32 v36, v36, s95, v3
	v_bfe_u32 v3, v45, 16, 1
	v_add3_u32 v3, v45, v3, s23
	v_bfe_u32 v37, v43, 16, 1
	v_lshrrev_b32_e32 v3, 16, v3
	v_add3_u32 v37, v43, v37, s23
	v_and_or_b32 v37, v37, s95, v3
	v_lshl_add_u64 v[38:39], v[32:33], 0, v[26:27]
	global_store_dwordx4 v[56:57], v[52:55], off
	global_store_dwordx4 v[38:39], v[34:37], off
	ds_read2_b32 v[38:39], v50 offset0:49 offset1:57
	ds_read2_b32 v[40:41], v50 offset0:16 offset1:24
	ds_read2_b32 v[42:43], v50 offset0:82 offset1:90
	ds_read2_b32 v[44:45], v50 offset0:115 offset1:123
	ds_read2_b32 v[46:47], v50 offset0:148 offset1:156
	ds_read2_b32 v[48:49], v50 offset0:181 offset1:189
	ds_read2_b32 v[52:53], v50 offset0:214 offset1:222
	ds_read2_b32 v[54:55], v50 offset0:247 offset1:255
	s_waitcnt lgkmcnt(7)
	v_bfe_u32 v34, v38, 16, 1
	s_waitcnt lgkmcnt(6)
	v_bfe_u32 v3, v40, 16, 1
	v_add3_u32 v3, v40, v3, s23
	v_lshrrev_b32_e32 v3, 16, v3
	v_add3_u32 v34, v38, v34, s23
	v_and_or_b32 v34, v34, s95, v3
	s_waitcnt lgkmcnt(5)
	v_bfe_u32 v3, v42, 16, 1
	v_add3_u32 v3, v42, v3, s23
	s_waitcnt lgkmcnt(4)
	v_bfe_u32 v35, v44, 16, 1
	v_lshrrev_b32_e32 v3, 16, v3
	v_add3_u32 v35, v44, v35, s23
	v_and_or_b32 v35, v35, s95, v3
	s_waitcnt lgkmcnt(3)
	v_bfe_u32 v3, v46, 16, 1
	v_add3_u32 v3, v46, v3, s23
	s_waitcnt lgkmcnt(2)
	v_bfe_u32 v36, v48, 16, 1
	v_lshrrev_b32_e32 v3, 16, v3
	v_add3_u32 v36, v48, v36, s23
	v_and_or_b32 v36, v36, s95, v3
	s_waitcnt lgkmcnt(1)
	v_bfe_u32 v3, v52, 16, 1
	v_add3_u32 v3, v52, v3, s23
	s_waitcnt lgkmcnt(0)
	v_bfe_u32 v37, v54, 16, 1
	v_lshrrev_b32_e32 v3, 16, v3
	v_add3_u32 v37, v54, v37, s23
	v_and_or_b32 v37, v37, s95, v3
	v_lshl_add_u64 v[56:57], v[32:33], 0, v[28:29]
	v_bfe_u32 v3, v41, 16, 1
	global_store_dwordx4 v[56:57], v[34:37], off
	v_add3_u32 v3, v41, v3, s23
	v_lshrrev_b32_e32 v3, 16, v3
	v_bfe_u32 v34, v39, 16, 1
	v_add3_u32 v34, v39, v34, s23
	v_and_or_b32 v34, v34, s95, v3
	v_bfe_u32 v3, v43, 16, 1
	v_add3_u32 v3, v43, v3, s23
	v_bfe_u32 v35, v45, 16, 1
	v_lshrrev_b32_e32 v3, 16, v3
	v_add3_u32 v35, v45, v35, s23
	v_and_or_b32 v35, v35, s95, v3
	v_bfe_u32 v3, v47, 16, 1
	v_add3_u32 v3, v47, v3, s23
	v_bfe_u32 v36, v49, 16, 1
	v_lshrrev_b32_e32 v3, 16, v3
	v_add3_u32 v36, v49, v36, s23
	v_and_or_b32 v36, v36, s95, v3
	v_bfe_u32 v3, v53, 16, 1
	v_add3_u32 v3, v53, v3, s23
	v_bfe_u32 v37, v55, 16, 1
	v_lshrrev_b32_e32 v3, 16, v3
	v_add3_u32 v37, v55, v37, s23
	v_and_or_b32 v37, v37, s95, v3
	v_lshl_add_u64 v[32:33], v[32:33], 0, v[30:31]
	global_store_dwordx4 v[32:33], v[34:37], off
	s_waitcnt lgkmcnt(0)
	s_branch .LBB0_819
